# UP epilogue de-serialised: row factors fetched with each 64-row group's first batch, vmcnt waits re-derived as counted waits at first use
# speedup vs baseline: 1.0058x; 1.0033x over previous
.LBB0_1923:
	s_lshl_b32 s11, s18, 8
	v_lshl_or_b32 v222, s19, 8, v243
	s_add_i32 s11, s11, s51
	v_ashrrev_i32_e32 v223, 31, v222
	v_or_b32_e32 v220, s11, v1
	v_lshlrev_b64 v[206:207], 1, v[222:223]
	s_and_b32 s13, s11, 0xfc0
	v_lshl_add_u64 v[224:225], s[4:5], 0, v[206:207]
	s_movk_i32 s21, 0x2c00
	s_cmp_lg_u32 s13, 0
	v_ashrrev_i32_e32 v221, 31, v220
	v_mad_i64_i32 v[36:37], s[18:19], v220, s21, v[224:225]
	v_lshl_add_u64 v[202:203], v[220:221], 2, s[6:7]
	s_cselect_b64 vcc, -1, 0
	global_load_dwordx4 v[164:167], v[36:37], off
	global_load_dword v186, v[202:203], off
	global_load_dword v227, v[202:203], off offset:64
	global_load_dword v228, v[202:203], off offset:128
	global_load_dword v229, v[202:203], off offset:192
	v_cndmask_b32_e32 v36, 0, v242, vcc
	v_add_u32_e32 v36, s11, v36
	v_mov_b64_e32 v[204:205], s[4:5]
	v_mad_i64_i32 v[36:37], s[18:19], v36, s21, v[204:205]
	v_lshl_add_u64 v[216:217], v[36:37], 0, v[206:207]
	global_load_dwordx4 v[182:185], v[216:217], off
	v_lshlrev_b64 v[36:37], 2, v[222:223]
	v_lshl_add_u64 v[208:209], v[178:179], 0, v[36:37]
	v_lshl_add_u64 v[38:39], v[194:195], 0, v[36:37]
	global_load_dwordx4 v[116:119], v[208:209], off
	global_load_dwordx4 v[128:131], v[38:39], off
	v_lshl_add_u64 v[40:41], v[196:197], 0, v[36:37]
	v_lshl_add_u64 v[210:211], v[180:181], 0, v[36:37]
	global_load_dwordx4 v[120:123], v[40:41], off
	global_load_dwordx4 v[124:127], v[210:211], off
	global_load_dwordx4 v[44:47], v[208:209], off offset:16
	global_load_dwordx4 v[48:51], v[38:39], off offset:16
	s_nop 0
	global_load_dwordx4 v[36:39], v[40:41], off offset:16
	s_nop 0
	global_load_dwordx4 v[40:43], v[210:211], off offset:16
	v_sub_u32_e32 v170, v220, v1
	v_and_b32_e32 v187, 0xfff, v170
	v_cmp_ne_u32_e32 vcc, 0, v187
	s_mov_b32 s20, 0xffff0000
	v_or_b32_e32 v212, 16, v220
	v_cndmask_b32_e64 v187, 0, -1, vcc
	v_cndmask_b32_e64 v223, 0, v187, s[38:39]
	v_cndmask_b32_e64 v245, 0, v187, s[36:37]
	v_mad_i64_i32 v[168:169], s[18:19], v212, s21, v[224:225]
	v_ashrrev_i32_e32 v213, 31, v212
	global_load_dwordx4 v[168:171], v[168:169], off
	s_addk_i32 s11, 0x80
	s_and_b32 s13, s11, 0xfc0
	s_cmp_lg_u32 s13, 0
	s_mov_b32 s25, 0x800000
	s_movk_i32 s24, 0x7200
	s_waitcnt lgkmcnt(0)
	s_waitcnt vmcnt(14)
	v_mov_b32_dpp v193, v164 row_shr:2 row_mask:0xf bank_mask:0xf bound_ctrl:1
	v_mov_b32_dpp v191, v164 row_shr:1 row_mask:0xf bank_mask:0xf bound_ctrl:1
	v_mov_b32_dpp v219, v165 row_shr:2 row_mask:0xf bank_mask:0xf bound_ctrl:1
	s_waitcnt vmcnt(13)
	v_pk_mul_f32 v[188:189], v[158:159], v[186:187] op_sel_hi:[1,0]
	v_pk_mul_f32 v[158:159], v[156:157], v[186:187] op_sel_hi:[1,0]
	v_lshlrev_b32_e32 v156, 16, v164
	v_and_b32_e32 v157, 0xffff0000, v164
	v_mov_b32_dpp v215, v165 row_shr:1 row_mask:0xf bank_mask:0xf bound_ctrl:1
	s_waitcnt vmcnt(9)
	v_and_b32_dpp v238, v182, v223 row_ror:2 row_mask:0xf bank_mask:0xf bound_ctrl:1
	v_and_b32_dpp v237, v182, v245 row_ror:1 row_mask:0xf bank_mask:0xf bound_ctrl:1
	v_and_b32_dpp v247, v184, v245 row_ror:1 row_mask:0xf bank_mask:0xf bound_ctrl:1
	v_and_b32_dpp v248, v184, v223 row_ror:2 row_mask:0xf bank_mask:0xf bound_ctrl:1
	v_and_b32_dpp v249, v185, v245 row_ror:1 row_mask:0xf bank_mask:0xf bound_ctrl:1
	v_and_b32_dpp v250, v185, v223 row_ror:2 row_mask:0xf bank_mask:0xf bound_ctrl:1
	v_or_b32_sdwa v184, v238, v193 dst_sel:WORD_1 dst_unused:UNUSED_PAD src0_sel:DWORD src1_sel:DWORD
	v_bitop3_b32 v185, v238, s20, v193 bitop3:0xc8
	v_and_b32_dpp v239, v183, v245 row_ror:1 row_mask:0xf bank_mask:0xf bound_ctrl:1
	v_and_b32_dpp v246, v183, v223 row_ror:2 row_mask:0xf bank_mask:0xf bound_ctrl:1
	v_or_b32_sdwa v182, v237, v191 dst_sel:WORD_1 dst_unused:UNUSED_PAD src0_sel:DWORD src1_sel:DWORD
	v_bitop3_b32 v183, v237, s20, v191 bitop3:0xc8
	s_waitcnt vmcnt(8)
	v_pk_mul_f32 v[184:185], v[116:117], v[184:185]
	v_or_b32_sdwa v192, v246, v219 dst_sel:WORD_1 dst_unused:UNUSED_PAD src0_sel:DWORD src1_sel:DWORD
	s_waitcnt vmcnt(7)
	v_pk_fma_f32 v[182:183], v[128:129], v[182:183], v[184:185]
	v_bitop3_b32 v193, v246, s20, v219 bitop3:0xc8
	s_waitcnt vmcnt(6)
	v_pk_fma_f32 v[156:157], v[120:121], v[156:157], v[182:183]
	v_or_b32_sdwa v190, v239, v215 dst_sel:WORD_1 dst_unused:UNUSED_PAD src0_sel:DWORD src1_sel:DWORD
	v_bitop3_b32 v191, v239, s20, v215 bitop3:0xc8
	v_pk_mul_f32 v[192:193], v[118:119], v[192:193]
	s_waitcnt vmcnt(5)
	v_pk_add_f32 v[156:157], v[124:125], v[156:157]
	v_pk_mul_f32 v[162:163], v[162:163], v[186:187] op_sel_hi:[1,0]
	v_pk_mul_f32 v[160:161], v[160:161], v[186:187] op_sel_hi:[1,0]
	v_lshlrev_b32_e32 v186, 16, v165
	v_and_b32_e32 v187, 0xffff0000, v165
	v_pk_fma_f32 v[184:185], v[130:131], v[190:191], v[192:193]
	v_mul_f32_e32 v182, 0xbfb8aa3b, v156
	v_mul_f32_e32 v183, 0xbfb8aa3b, v157
	v_exp_f32_e32 v190, v182
	v_exp_f32_e32 v191, v183
	v_pk_fma_f32 v[182:183], v[122:123], v[186:187], v[184:185]
	v_mov_b32_dpp v233, v166 row_shr:2 row_mask:0xf bank_mask:0xf bound_ctrl:1
	v_pk_add_f32 v[182:183], v[126:127], v[182:183]
	v_add_f32_e32 v184, 1.0, v190
	v_mul_f32_e32 v186, 0xbfb8aa3b, v182
	v_mul_f32_e32 v187, 0xbfb8aa3b, v183
	v_exp_f32_e32 v186, v186
	v_exp_f32_e32 v187, v187
	v_add_f32_e32 v185, 1.0, v191
	v_rcp_f32_e32 v184, v184
	v_rcp_f32_e32 v185, v185
	v_add_f32_e32 v186, 1.0, v186
	v_add_f32_e32 v187, 1.0, v187
	v_rcp_f32_e32 v186, v186
	v_rcp_f32_e32 v187, v187
	v_pk_mul_f32 v[156:157], v[156:157], v[184:185]
	v_mov_b32_dpp v221, v166 row_shr:1 row_mask:0xf bank_mask:0xf bound_ctrl:1
	v_or_b32_sdwa v218, v248, v233 dst_sel:WORD_1 dst_unused:UNUSED_PAD src0_sel:DWORD src1_sel:DWORD
	v_bitop3_b32 v219, v248, s20, v233 bitop3:0xc8
	v_pk_mul_f32 v[156:157], v[156:157], v[160:161]
	v_pk_mul_f32 v[160:161], v[182:183], v[186:187]
	v_or_b32_sdwa v214, v247, v221 dst_sel:WORD_1 dst_unused:UNUSED_PAD src0_sel:DWORD src1_sel:DWORD
	v_bitop3_b32 v215, v247, s20, v221 bitop3:0xc8
	v_pk_mul_f32 v[160:161], v[160:161], v[162:163]
	s_waitcnt vmcnt(4)
	v_pk_mul_f32 v[162:163], v[44:45], v[218:219]
	v_lshlrev_b32_e32 v182, 16, v166
	s_waitcnt vmcnt(3)
	v_pk_fma_f32 v[162:163], v[48:49], v[214:215], v[162:163]
	v_and_b32_e32 v183, 0xffff0000, v166
	s_waitcnt vmcnt(2)
	v_pk_fma_f32 v[162:163], v[36:37], v[182:183], v[162:163]
	v_cvt_pk_bf16_f32 v156, v156, v157
	s_waitcnt vmcnt(1)
	v_pk_add_f32 v[162:163], v[40:41], v[162:163]
	v_mov_b32_dpp v235, v167 row_shr:2 row_mask:0xf bank_mask:0xf bound_ctrl:1
	v_mul_f32_e32 v157, 0xbfb8aa3b, v162
	v_exp_f32_e32 v182, v157
	v_mul_f32_e32 v157, 0xbfb8aa3b, v163
	v_exp_f32_e32 v183, v157
	v_mov_b32_dpp v236, v167 row_shr:1 row_mask:0xf bank_mask:0xf bound_ctrl:1
	v_or_b32_sdwa v234, v250, v235 dst_sel:WORD_1 dst_unused:UNUSED_PAD src0_sel:DWORD src1_sel:DWORD
	v_bitop3_b32 v235, v250, s20, v235 bitop3:0xc8
	v_or_b32_sdwa v232, v249, v236 dst_sel:WORD_1 dst_unused:UNUSED_PAD src0_sel:DWORD src1_sel:DWORD
	v_bitop3_b32 v233, v249, s20, v236 bitop3:0xc8
	v_cvt_pk_bf16_f32 v157, v160, v161
	v_add_f32_e32 v160, 1.0, v182
	v_add_f32_e32 v161, 1.0, v183
	v_pk_mul_f32 v[182:183], v[46:47], v[234:235]
	v_lshlrev_b32_e32 v184, 16, v167
	v_pk_fma_f32 v[182:183], v[50:51], v[232:233], v[182:183]
	v_and_b32_e32 v185, 0xffff0000, v167
	v_pk_fma_f32 v[182:183], v[38:39], v[184:185], v[182:183]
	v_rcp_f32_e32 v160, v160
	v_pk_add_f32 v[182:183], v[42:43], v[182:183]
	v_rcp_f32_e32 v161, v161
	v_mul_f32_e32 v184, 0xbfb8aa3b, v182
	v_mul_f32_e32 v185, 0xbfb8aa3b, v183
	v_exp_f32_e32 v184, v184
	v_exp_f32_e32 v185, v185
	v_pk_mul_f32 v[160:161], v[162:163], v[160:161]
	v_mov_b64_e32 v[218:219], s[2:3]
	v_add_f32_e32 v184, 1.0, v184
	v_add_f32_e32 v185, 1.0, v185
	v_rcp_f32_e32 v184, v184
	v_rcp_f32_e32 v185, v185
	v_pk_mul_f32 v[158:159], v[158:159], v[160:161]
	v_lshl_add_u64 v[214:215], v[212:213], 2, s[6:7]
	v_cvt_pk_bf16_f32 v158, v158, v159
	v_pk_mul_f32 v[160:161], v[182:183], v[184:185]
	v_sub_u32_e32 v183, v212, v1
	v_pk_mul_f32 v[160:161], v[188:189], v[160:161]
	v_and_b32_e32 v183, 0xfdf, v183
	v_cvt_pk_bf16_f32 v159, v160, v161
	v_mad_i64_i32 v[160:161], s[18:19], v220, s21, v[218:219]
	v_lshl_add_u64 v[162:163], v[160:161], 0, v[206:207]
	global_store_dwordx4 v[162:163], v[156:159], off
	v_mov_b32_e32 v182, v227
	v_cmp_ne_u32_e32 vcc, 0, v183
	s_waitcnt vmcnt(1)
	v_mov_b32_dpp v185, v168 row_shr:2 row_mask:0xf bank_mask:0xf bound_ctrl:1
	v_mov_b32_dpp v191, v169 row_shr:1 row_mask:0xf bank_mask:0xf bound_ctrl:1
	v_cndmask_b32_e64 v183, 0, -1, vcc
	v_cndmask_b32_e64 v213, 0, v183, s[38:39]
	v_cndmask_b32_e64 v221, 0, v183, s[36:37]
	v_mov_b32_dpp v183, v168 row_shr:1 row_mask:0xf bank_mask:0xf bound_ctrl:1
	v_and_b32_dpp v189, v164, v213 row_ror:2 row_mask:0xf bank_mask:0xf bound_ctrl:1
	v_and_b32_dpp v187, v164, v221 row_ror:1 row_mask:0xf bank_mask:0xf bound_ctrl:1
	v_or_b32_sdwa v164, v189, v185 dst_sel:WORD_1 dst_unused:UNUSED_PAD src0_sel:DWORD src1_sel:DWORD
	v_mov_b32_dpp v193, v169 row_shr:2 row_mask:0xf bank_mask:0xf bound_ctrl:1
	v_and_b32_dpp v233, v165, v221 row_ror:1 row_mask:0xf bank_mask:0xf bound_ctrl:1
	v_and_b32_dpp v234, v165, v213 row_ror:2 row_mask:0xf bank_mask:0xf bound_ctrl:1
	v_mov_b32_dpp v235, v170 row_shr:1 row_mask:0xf bank_mask:0xf bound_ctrl:1
	v_and_b32_dpp v237, v166, v221 row_ror:1 row_mask:0xf bank_mask:0xf bound_ctrl:1
	v_bitop3_b32 v165, v189, s20, v185 bitop3:0xc8
	v_or_b32_sdwa v184, v187, v183 dst_sel:WORD_1 dst_unused:UNUSED_PAD src0_sel:DWORD src1_sel:DWORD
	v_or_b32_sdwa v186, v233, v191 dst_sel:WORD_1 dst_unused:UNUSED_PAD src0_sel:DWORD src1_sel:DWORD
	v_or_b32_sdwa v188, v234, v193 dst_sel:WORD_1 dst_unused:UNUSED_PAD src0_sel:DWORD src1_sel:DWORD
	v_or_b32_sdwa v190, v237, v235 dst_sel:WORD_1 dst_unused:UNUSED_PAD src0_sel:DWORD src1_sel:DWORD
	v_bitop3_b32 v185, v187, s20, v183 bitop3:0xc8
	v_bitop3_b32 v189, v234, s20, v193 bitop3:0xc8
	v_bitop3_b32 v187, v233, s20, v191 bitop3:0xc8
	v_bitop3_b32 v191, v237, s20, v235 bitop3:0xc8
	v_mov_b32_dpp v236, v170 row_shr:2 row_mask:0xf bank_mask:0xf bound_ctrl:1
	v_and_b32_dpp v238, v166, v213 row_ror:2 row_mask:0xf bank_mask:0xf bound_ctrl:1
	v_or_b32_sdwa v166, v238, v236 dst_sel:WORD_1 dst_unused:UNUSED_PAD src0_sel:DWORD src1_sel:DWORD
	v_and_b32_dpp v247, v167, v221 row_ror:1 row_mask:0xf bank_mask:0xf bound_ctrl:1
	v_and_b32_dpp v248, v167, v213 row_ror:2 row_mask:0xf bank_mask:0xf bound_ctrl:1
	v_bitop3_b32 v167, v238, s20, v236 bitop3:0xc8
	v_mov_b32_dpp v246, v171 row_shr:2 row_mask:0xf bank_mask:0xf bound_ctrl:1
	v_mov_b32_dpp v239, v171 row_shr:1 row_mask:0xf bank_mask:0xf bound_ctrl:1
	v_or_b32_sdwa v232, v248, v246 dst_sel:WORD_1 dst_unused:UNUSED_PAD src0_sel:DWORD src1_sel:DWORD
	v_bitop3_b32 v233, v248, s20, v246 bitop3:0xc8
	v_or_b32_sdwa v192, v247, v239 dst_sel:WORD_1 dst_unused:UNUSED_PAD src0_sel:DWORD src1_sel:DWORD
	v_bitop3_b32 v193, v247, s20, v239 bitop3:0xc8
	v_or_b32_e32 v160, 32, v220
	v_mad_i64_i32 v[156:157], s[18:19], v160, s21, v[224:225]
	global_load_dwordx4 v[156:159], v[156:157], off
	v_ashrrev_i32_e32 v161, 31, v160
	s_waitcnt lgkmcnt(0)
	v_pk_mul_f32 v[234:235], v[150:151], v[182:183] op_sel_hi:[1,0]
	v_pk_mul_f32 v[150:151], v[116:117], v[164:165]
	v_pk_mul_f32 v[154:155], v[154:155], v[182:183] op_sel_hi:[1,0]
	v_pk_mul_f32 v[152:153], v[152:153], v[182:183] op_sel_hi:[1,0]
	v_pk_fma_f32 v[150:151], v[128:129], v[184:185], v[150:151]
	v_lshlrev_b32_e32 v164, 16, v168
	v_and_b32_e32 v165, 0xffff0000, v168
	v_pk_mul_f32 v[148:149], v[148:149], v[182:183] op_sel_hi:[1,0]
	v_pk_mul_f32 v[182:183], v[118:119], v[188:189]
	v_pk_fma_f32 v[150:151], v[120:121], v[164:165], v[150:151]
	v_pk_fma_f32 v[182:183], v[130:131], v[186:187], v[182:183]
	v_lshlrev_b32_e32 v184, 16, v169
	v_and_b32_e32 v185, 0xffff0000, v169
	v_pk_add_f32 v[150:151], v[124:125], v[150:151]
	v_pk_fma_f32 v[182:183], v[122:123], v[184:185], v[182:183]
	v_mul_f32_e32 v164, 0xbfb8aa3b, v150
	v_mul_f32_e32 v165, 0xbfb8aa3b, v151
	v_pk_add_f32 v[182:183], v[126:127], v[182:183]
	v_exp_f32_e32 v164, v164
	v_exp_f32_e32 v165, v165
	v_mul_f32_e32 v184, 0xbfb8aa3b, v182
	v_mul_f32_e32 v185, 0xbfb8aa3b, v183
	v_exp_f32_e32 v184, v184
	v_exp_f32_e32 v185, v185
	v_add_f32_e32 v164, 1.0, v164
	v_add_f32_e32 v165, 1.0, v165
	v_rcp_f32_e32 v164, v164
	v_rcp_f32_e32 v165, v165
	v_add_f32_e32 v184, 1.0, v184
	v_add_f32_e32 v185, 1.0, v185
	v_rcp_f32_e32 v184, v184
	v_rcp_f32_e32 v185, v185
	v_pk_mul_f32 v[150:151], v[150:151], v[164:165]
	v_lshlrev_b32_e32 v164, 16, v170
	v_pk_mul_f32 v[150:151], v[150:151], v[152:153]
	v_pk_mul_f32 v[152:153], v[182:183], v[184:185]
	v_and_b32_e32 v165, 0xffff0000, v170
	v_pk_mul_f32 v[152:153], v[152:153], v[154:155]
	v_pk_mul_f32 v[154:155], v[44:45], v[166:167]
	v_cvt_pk_bf16_f32 v150, v150, v151
	v_pk_fma_f32 v[154:155], v[48:49], v[190:191], v[154:155]
	v_lshlrev_b32_e32 v166, 16, v171
	v_pk_fma_f32 v[154:155], v[36:37], v[164:165], v[154:155]
	v_and_b32_e32 v167, 0xffff0000, v171
	v_pk_add_f32 v[154:155], v[40:41], v[154:155]
	s_nop 0
	v_mul_f32_e32 v151, 0xbfb8aa3b, v154
	v_exp_f32_e32 v164, v151
	v_mul_f32_e32 v151, 0xbfb8aa3b, v155
	v_exp_f32_e32 v165, v151
	v_cvt_pk_bf16_f32 v151, v152, v153
	v_add_f32_e32 v152, 1.0, v164
	v_rcp_f32_e32 v152, v152
	v_add_f32_e32 v153, 1.0, v165
	v_pk_mul_f32 v[164:165], v[46:47], v[232:233]
	v_rcp_f32_e32 v153, v153
	v_pk_fma_f32 v[164:165], v[50:51], v[192:193], v[164:165]
	v_pk_mul_f32 v[152:153], v[154:155], v[152:153]
	v_pk_fma_f32 v[164:165], v[38:39], v[166:167], v[164:165]
	v_pk_mul_f32 v[148:149], v[148:149], v[152:153]
	v_pk_add_f32 v[164:165], v[42:43], v[164:165]
	v_cvt_pk_bf16_f32 v152, v148, v149
	v_mul_f32_e32 v166, 0xbfb8aa3b, v164
	v_mul_f32_e32 v167, 0xbfb8aa3b, v165
	v_exp_f32_e32 v166, v166
	v_exp_f32_e32 v167, v167
	v_sub_u32_e32 v155, v160, v1
	v_and_b32_e32 v155, 0xfff, v155
	v_add_f32_e32 v166, 1.0, v166
	v_add_f32_e32 v167, 1.0, v167
	v_rcp_f32_e32 v166, v166
	v_rcp_f32_e32 v167, v167
	v_cmp_ne_u32_e32 vcc, 0, v155
	v_pk_mul_f32 v[148:149], v[164:165], v[166:167]
	s_nop 0
	v_pk_mul_f32 v[148:149], v[234:235], v[148:149]
	v_cndmask_b32_e64 v155, 0, -1, vcc
	v_cvt_pk_bf16_f32 v153, v148, v149
	v_mad_i64_i32 v[148:149], s[18:19], v212, s21, v[218:219]
	v_lshl_add_u64 v[148:149], v[148:149], 0, v[206:207]
	global_store_dwordx4 v[148:149], v[150:153], off
	s_cselect_b64 vcc, -1, 0
	s_nop 0
	v_lshl_add_u64 v[150:151], v[160:161], 2, s[6:7]
	v_mov_b32_e32 v154, v228
	v_or_b32_e32 v152, 48, v220
	v_mad_i64_i32 v[164:165], s[18:19], v152, s21, v[224:225]
	v_cndmask_b32_e64 v161, 0, v155, s[38:39]
	global_load_dwordx4 v[182:185], v[164:165], off
	v_cndmask_b32_e64 v164, 0, v155, s[36:37]
	s_waitcnt vmcnt(2)
	v_mov_b32_dpp v165, v156 row_shr:2 row_mask:0xf bank_mask:0xf bound_ctrl:1
	v_and_b32_dpp v187, v168, v161 row_ror:2 row_mask:0xf bank_mask:0xf bound_ctrl:1
	v_mov_b32_dpp v155, v156 row_shr:1 row_mask:0xf bank_mask:0xf bound_ctrl:1
	v_and_b32_dpp v167, v168, v164 row_ror:1 row_mask:0xf bank_mask:0xf bound_ctrl:1
	v_or_b32_sdwa v168, v187, v165 dst_sel:WORD_1 dst_unused:UNUSED_PAD src0_sel:DWORD src1_sel:DWORD
	v_and_b32_dpp v193, v169, v164 row_ror:1 row_mask:0xf bank_mask:0xf bound_ctrl:1
	v_and_b32_dpp v233, v169, v161 row_ror:2 row_mask:0xf bank_mask:0xf bound_ctrl:1
	v_bitop3_b32 v169, v187, s20, v165 bitop3:0xc8
	v_or_b32_sdwa v166, v167, v155 dst_sel:WORD_1 dst_unused:UNUSED_PAD src0_sel:DWORD src1_sel:DWORD
	v_bitop3_b32 v167, v167, s20, v155 bitop3:0xc8
	v_pk_mul_f32 v[168:169], v[116:117], v[168:169]
	v_mov_b32_dpp v189, v157 row_shr:2 row_mask:0xf bank_mask:0xf bound_ctrl:1
	v_pk_fma_f32 v[166:167], v[128:129], v[166:167], v[168:169]
	v_lshlrev_b32_e32 v168, 16, v156
	v_and_b32_e32 v169, 0xffff0000, v156
	v_pk_fma_f32 v[166:167], v[120:121], v[168:169], v[166:167]
	v_mov_b32_dpp v191, v157 row_shr:1 row_mask:0xf bank_mask:0xf bound_ctrl:1
	v_pk_add_f32 v[166:167], v[124:125], v[166:167]
	v_or_b32_sdwa v188, v233, v189 dst_sel:WORD_1 dst_unused:UNUSED_PAD src0_sel:DWORD src1_sel:DWORD
	v_bitop3_b32 v189, v233, s20, v189 bitop3:0xc8
	v_mul_f32_e32 v165, 0xbfb8aa3b, v167
	v_or_b32_sdwa v186, v193, v191 dst_sel:WORD_1 dst_unused:UNUSED_PAD src0_sel:DWORD src1_sel:DWORD
	v_bitop3_b32 v187, v193, s20, v191 bitop3:0xc8
	v_exp_f32_e32 v165, v165
	v_pk_mul_f32 v[168:169], v[118:119], v[188:189]
	v_mov_b32_dpp v235, v158 row_shr:2 row_mask:0xf bank_mask:0xf bound_ctrl:1
	v_pk_fma_f32 v[168:169], v[130:131], v[186:187], v[168:169]
	v_lshlrev_b32_e32 v186, 16, v157
	v_and_b32_e32 v187, 0xffff0000, v157
	v_pk_fma_f32 v[168:169], v[122:123], v[186:187], v[168:169]
	v_and_b32_dpp v237, v170, v161 row_ror:2 row_mask:0xf bank_mask:0xf bound_ctrl:1
	v_pk_add_f32 v[168:169], v[126:127], v[168:169]
	v_mov_b32_dpp v234, v158 row_shr:1 row_mask:0xf bank_mask:0xf bound_ctrl:1
	v_mul_f32_e32 v186, 0xbfb8aa3b, v169
	v_exp_f32_e32 v187, v186
	v_and_b32_dpp v236, v170, v164 row_ror:1 row_mask:0xf bank_mask:0xf bound_ctrl:1
	v_or_b32_sdwa v170, v237, v235 dst_sel:WORD_1 dst_unused:UNUSED_PAD src0_sel:DWORD src1_sel:DWORD
	v_and_b32_dpp v246, v171, v164 row_ror:1 row_mask:0xf bank_mask:0xf bound_ctrl:1
	v_and_b32_dpp v247, v171, v161 row_ror:2 row_mask:0xf bank_mask:0xf bound_ctrl:1
	v_bitop3_b32 v171, v237, s20, v235 bitop3:0xc8
	v_or_b32_sdwa v190, v236, v234 dst_sel:WORD_1 dst_unused:UNUSED_PAD src0_sel:DWORD src1_sel:DWORD
	v_bitop3_b32 v191, v236, s20, v234 bitop3:0xc8
	v_mov_b32_dpp v239, v159 row_shr:2 row_mask:0xf bank_mask:0xf bound_ctrl:1
	v_mov_b32_dpp v238, v159 row_shr:1 row_mask:0xf bank_mask:0xf bound_ctrl:1
	v_or_b32_sdwa v232, v247, v239 dst_sel:WORD_1 dst_unused:UNUSED_PAD src0_sel:DWORD src1_sel:DWORD
	v_bitop3_b32 v233, v247, s20, v239 bitop3:0xc8
	v_or_b32_sdwa v192, v246, v238 dst_sel:WORD_1 dst_unused:UNUSED_PAD src0_sel:DWORD src1_sel:DWORD
	v_bitop3_b32 v193, v246, s20, v238 bitop3:0xc8
	v_ashrrev_i32_e32 v153, 31, v152
	s_waitcnt lgkmcnt(0)
	v_pk_mul_f32 v[146:147], v[146:147], v[154:155] op_sel_hi:[1,0]
	v_pk_mul_f32 v[144:145], v[144:145], v[154:155] op_sel_hi:[1,0]
	v_pk_mul_f32 v[142:143], v[142:143], v[154:155] op_sel_hi:[1,0]
	v_mul_f32_e32 v155, 0xbfb8aa3b, v166
	v_exp_f32_e32 v155, v155
	s_waitcnt vmcnt(0)
	v_mov_b32_dpp v188, v184 row_shr:2 row_mask:0xf bank_mask:0xf bound_ctrl:1
	v_pk_mul_f32 v[140:141], v[140:141], v[154:155] op_sel_hi:[1,0]
	v_add_f32_e32 v154, 1.0, v155
	v_add_f32_e32 v155, 1.0, v165
	v_mul_f32_e32 v165, 0xbfb8aa3b, v168
	v_exp_f32_e32 v165, v165
	v_rcp_f32_e32 v154, v154
	v_rcp_f32_e32 v155, v155
	v_add_f32_e32 v165, 1.0, v165
	v_rcp_f32_e32 v186, v165
	v_add_f32_e32 v165, 1.0, v187
	v_rcp_f32_e32 v187, v165
	v_pk_mul_f32 v[154:155], v[166:167], v[154:155]
	v_lshlrev_b32_e32 v166, 16, v158
	v_pk_mul_f32 v[144:145], v[154:155], v[144:145]
	v_pk_mul_f32 v[154:155], v[168:169], v[186:187]
	v_and_b32_e32 v167, 0xffff0000, v158
	v_pk_mul_f32 v[146:147], v[154:155], v[146:147]
	v_pk_mul_f32 v[154:155], v[44:45], v[170:171]
	v_cvt_pk_bf16_f32 v144, v144, v145
	v_pk_fma_f32 v[154:155], v[48:49], v[190:191], v[154:155]
	v_lshlrev_b32_e32 v168, 16, v159
	v_pk_fma_f32 v[154:155], v[36:37], v[166:167], v[154:155]
	v_and_b32_e32 v169, 0xffff0000, v159
	v_pk_add_f32 v[154:155], v[40:41], v[154:155]
	v_mov_b32_dpp v187, v184 row_shr:1 row_mask:0xf bank_mask:0xf bound_ctrl:1
	v_mul_f32_e32 v145, 0xbfb8aa3b, v154
	v_exp_f32_e32 v165, v145
	v_mul_f32_e32 v145, 0xbfb8aa3b, v155
	v_exp_f32_e32 v166, v145
	v_cvt_pk_bf16_f32 v145, v146, v147
	v_add_f32_e32 v146, 1.0, v165
	v_rcp_f32_e32 v146, v146
	v_add_f32_e32 v147, 1.0, v166
	v_pk_mul_f32 v[166:167], v[46:47], v[232:233]
	v_rcp_f32_e32 v147, v147
	v_pk_fma_f32 v[166:167], v[50:51], v[192:193], v[166:167]
	v_mov_b32_dpp v192, v185 row_shr:2 row_mask:0xf bank_mask:0xf bound_ctrl:1
	v_pk_fma_f32 v[166:167], v[38:39], v[168:169], v[166:167]
	v_pk_mul_f32 v[146:147], v[154:155], v[146:147]
	v_pk_add_f32 v[166:167], v[42:43], v[166:167]
	v_pk_mul_f32 v[140:141], v[140:141], v[146:147]
	v_mul_f32_e32 v165, 0xbfb8aa3b, v166
	v_exp_f32_e32 v165, v165
	v_mul_f32_e32 v168, 0xbfb8aa3b, v167
	v_exp_f32_e32 v169, v168
	v_cvt_pk_bf16_f32 v146, v140, v141
	v_add_f32_e32 v165, 1.0, v165
	v_rcp_f32_e32 v168, v165
	v_add_f32_e32 v165, 1.0, v169
	v_rcp_f32_e32 v169, v165
	v_mov_b32_dpp v155, v157 row_ror:1 row_mask:0xf bank_mask:0xf bound_ctrl:1
	v_cndmask_b32_e64 v171, 0, v155, s[36:37]
	v_mov_b32_dpp v157, v157 row_ror:2 row_mask:0xf bank_mask:0xf bound_ctrl:1
	v_pk_mul_f32 v[140:141], v[166:167], v[168:169]
	v_mov_b32_dpp v155, v158 row_ror:1 row_mask:0xf bank_mask:0xf bound_ctrl:1
	v_pk_mul_f32 v[140:141], v[142:143], v[140:141]
	v_mov_b32_dpp v168, v158 row_ror:2 row_mask:0xf bank_mask:0xf bound_ctrl:1
	v_cvt_pk_bf16_f32 v147, v140, v141
	v_mad_i64_i32 v[140:141], s[18:19], v160, s21, v[218:219]
	v_lshl_add_u64 v[142:143], v[140:141], 0, v[206:207]
	global_store_dwordx4 v[142:143], v[144:147], off
	v_cndmask_b32_e64 v189, 0, v155, s[36:37]
	v_mov_b32_dpp v155, v159 row_ror:1 row_mask:0xf bank_mask:0xf bound_ctrl:1
	v_lshl_add_u64 v[144:145], v[152:153], 2, s[6:7]
	v_mov_b32_e32 v140, v229
	v_mov_b32_dpp v153, v156 row_ror:2 row_mask:0xf bank_mask:0xf bound_ctrl:1
	v_mov_b32_dpp v146, v156 row_ror:1 row_mask:0xf bank_mask:0xf bound_ctrl:1
	v_mov_b32_dpp v147, v182 row_shr:2 row_mask:0xf bank_mask:0xf bound_ctrl:1
	v_cndmask_b32_e64 v153, 0, v153, s[38:39]
	v_mov_b32_dpp v141, v182 row_shr:1 row_mask:0xf bank_mask:0xf bound_ctrl:1
	v_cndmask_b32_e64 v165, 0, v146, s[36:37]
	v_or_b32_sdwa v154, v153, v147 dst_sel:WORD_1 dst_unused:UNUSED_PAD src0_sel:DWORD src1_sel:DWORD
	v_mov_b32_dpp v169, v183 row_shr:1 row_mask:0xf bank_mask:0xf bound_ctrl:1
	v_mov_b32_dpp v167, v183 row_shr:2 row_mask:0xf bank_mask:0xf bound_ctrl:1
	v_cndmask_b32_e64 v157, 0, v157, s[38:39]
	v_cndmask_b32_e64 v190, 0, v168, s[38:39]
	v_mov_b32_dpp v159, v159 row_ror:2 row_mask:0xf bank_mask:0xf bound_ctrl:1
	v_cndmask_b32_e64 v193, 0, v155, s[36:37]
	v_bitop3_b32 v155, v153, s20, v147 bitop3:0xc8
	v_or_b32_sdwa v146, v165, v141 dst_sel:WORD_1 dst_unused:UNUSED_PAD src0_sel:DWORD src1_sel:DWORD
	v_or_b32_sdwa v156, v171, v169 dst_sel:WORD_1 dst_unused:UNUSED_PAD src0_sel:DWORD src1_sel:DWORD
	v_or_b32_sdwa v166, v157, v167 dst_sel:WORD_1 dst_unused:UNUSED_PAD src0_sel:DWORD src1_sel:DWORD
	v_or_b32_sdwa v158, v189, v187 dst_sel:WORD_1 dst_unused:UNUSED_PAD src0_sel:DWORD src1_sel:DWORD
	v_or_b32_sdwa v168, v190, v188 dst_sel:WORD_1 dst_unused:UNUSED_PAD src0_sel:DWORD src1_sel:DWORD
	v_cndmask_b32_e64 v232, 0, v159, s[38:39]
	v_bitop3_b32 v147, v165, s20, v141 bitop3:0xc8
	v_bitop3_b32 v167, v157, s20, v167 bitop3:0xc8
	v_bitop3_b32 v157, v171, s20, v169 bitop3:0xc8
	v_bitop3_b32 v169, v190, s20, v188 bitop3:0xc8
	v_bitop3_b32 v159, v189, s20, v187 bitop3:0xc8
	v_mov_b32_dpp v191, v185 row_shr:1 row_mask:0xf bank_mask:0xf bound_ctrl:1
	v_or_b32_sdwa v186, v232, v192 dst_sel:WORD_1 dst_unused:UNUSED_PAD src0_sel:DWORD src1_sel:DWORD
	v_bitop3_b32 v187, v232, s20, v192 bitop3:0xc8
	v_or_b32_sdwa v170, v193, v191 dst_sel:WORD_1 dst_unused:UNUSED_PAD src0_sel:DWORD src1_sel:DWORD
	v_bitop3_b32 v171, v193, s20, v191 bitop3:0xc8
	v_add_u32_e32 v165, 0x80, v220
	s_waitcnt lgkmcnt(0)
	v_pk_mul_f32 v[188:189], v[134:135], v[140:141] op_sel_hi:[1,0]
	v_pk_mul_f32 v[134:135], v[116:117], v[154:155]
	v_pk_mul_f32 v[138:139], v[138:139], v[140:141] op_sel_hi:[1,0]
	v_pk_fma_f32 v[134:135], v[128:129], v[146:147], v[134:135]
	v_lshlrev_b32_e32 v146, 16, v182
	v_and_b32_e32 v147, 0xffff0000, v182
	v_pk_fma_f32 v[134:135], v[120:121], v[146:147], v[134:135]
	v_pk_mul_f32 v[136:137], v[136:137], v[140:141] op_sel_hi:[1,0]
	v_pk_add_f32 v[134:135], v[124:125], v[134:135]
	v_lshlrev_b32_e32 v154, 16, v183
	v_mul_f32_e32 v141, 0xbfb8aa3b, v134
	v_exp_f32_e32 v146, v141
	v_mul_f32_e32 v141, 0xbfb8aa3b, v135
	v_exp_f32_e32 v147, v141
	v_pk_mul_f32 v[140:141], v[132:133], v[140:141] op_sel_hi:[1,0]
	v_add_f32_e32 v132, 1.0, v146
	v_and_b32_e32 v155, 0xffff0000, v183
	v_add_f32_e32 v133, 1.0, v147
	v_pk_mul_f32 v[146:147], v[118:119], v[166:167]
	v_rcp_f32_e32 v132, v132
	v_pk_fma_f32 v[146:147], v[130:131], v[156:157], v[146:147]
	v_rcp_f32_e32 v133, v133
	v_pk_fma_f32 v[146:147], v[122:123], v[154:155], v[146:147]
	v_pk_mul_f32 v[132:133], v[134:135], v[132:133]
	v_pk_add_f32 v[146:147], v[126:127], v[146:147]
	v_pk_mul_f32 v[132:133], v[132:133], v[136:137]
	v_mul_f32_e32 v153, 0xbfb8aa3b, v146
	v_exp_f32_e32 v153, v153
	v_mul_f32_e32 v154, 0xbfb8aa3b, v147
	v_exp_f32_e32 v155, v154
	v_pk_mul_f32 v[136:137], v[44:45], v[168:169]
	v_add_f32_e32 v153, 1.0, v153
	v_rcp_f32_e32 v154, v153
	v_add_f32_e32 v153, 1.0, v155
	v_rcp_f32_e32 v155, v153
	v_pk_fma_f32 v[136:137], v[48:49], v[158:159], v[136:137]
	v_cvt_pk_bf16_f32 v132, v132, v133
	v_add_u32_e32 v159, 0x90, v220
	v_pk_mul_f32 v[134:135], v[146:147], v[154:155]
	v_lshlrev_b32_e32 v146, 16, v185
	v_pk_mul_f32 v[134:135], v[134:135], v[138:139]
	v_lshlrev_b32_e32 v138, 16, v184
	v_and_b32_e32 v139, 0xffff0000, v184
	v_pk_fma_f32 v[136:137], v[36:37], v[138:139], v[136:137]
	v_and_b32_e32 v147, 0xffff0000, v185
	v_pk_add_f32 v[136:137], v[40:41], v[136:137]
	s_nop 0
	v_mul_f32_e32 v133, 0xbfb8aa3b, v136
	v_exp_f32_e32 v138, v133
	v_mul_f32_e32 v133, 0xbfb8aa3b, v137
	v_exp_f32_e32 v139, v133
	v_cvt_pk_bf16_f32 v133, v134, v135
	v_add_f32_e32 v134, 1.0, v138
	v_rcp_f32_e32 v134, v134
	v_add_f32_e32 v135, 1.0, v139
	v_pk_mul_f32 v[138:139], v[46:47], v[186:187]
	v_rcp_f32_e32 v135, v135
	v_pk_fma_f32 v[138:139], v[50:51], v[170:171], v[138:139]
	v_pk_mul_f32 v[134:135], v[136:137], v[134:135]
	v_pk_fma_f32 v[138:139], v[38:39], v[146:147], v[138:139]
	v_pk_mul_f32 v[134:135], v[140:141], v[134:135]
	v_pk_add_f32 v[138:139], v[42:43], v[138:139]
	v_cvt_pk_bf16_f32 v134, v134, v135
	v_mul_f32_e32 v146, 0xbfb8aa3b, v138
	v_mul_f32_e32 v147, 0xbfb8aa3b, v139
	v_exp_f32_e32 v146, v146
	v_exp_f32_e32 v147, v147
	v_add_f32_e32 v146, 1.0, v146
	v_add_f32_e32 v147, 1.0, v147
	v_rcp_f32_e32 v146, v146
	v_rcp_f32_e32 v147, v147
	s_nop 0
	v_pk_mul_f32 v[136:137], v[138:139], v[146:147]
	s_nop 0
	v_pk_mul_f32 v[136:137], v[188:189], v[136:137]
	v_sub_u32_e32 v139, v165, v1
	v_cvt_pk_bf16_f32 v135, v136, v137
	v_mad_i64_i32 v[136:137], s[18:19], v152, s21, v[218:219]
	v_lshl_add_u64 v[136:137], v[136:137], 0, v[206:207]
	global_store_dwordx4 v[136:137], v[132:135], off
	v_and_b32_e32 v139, 0xfff, v139
	s_nop 0
	v_cndmask_b32_e32 v132, 0, v242, vcc
	v_add_u32_e32 v132, s11, v132
	v_mad_i64_i32 v[132:133], s[18:19], v132, s21, v[204:205]
	v_mad_i64_i32 v[134:135], s[18:19], v165, s21, v[224:225]
	global_load_dwordx4 v[166:169], v[134:135], off
	v_lshl_add_u64 v[140:141], v[132:133], 0, v[206:207]
	global_load_dwordx4 v[182:185], v[140:141], off
	global_load_dword v138, v[202:203], off offset:512
	global_load_dword v227, v[202:203], off offset:576
	global_load_dword v228, v[202:203], off offset:640
	global_load_dword v229, v[202:203], off offset:704
	v_cmp_ne_u32_e32 vcc, 0, v139
	v_mad_i64_i32 v[132:133], s[18:19], v159, s21, v[224:225]
	s_nop 0
	v_cndmask_b32_e64 v139, 0, -1, vcc
	v_cndmask_b32_e64 v157, 0, v139, s[38:39]
	v_cndmask_b32_e64 v158, 0, v139, s[36:37]
	global_load_dwordx4 v[132:135], v[132:133], off
	s_waitcnt lgkmcnt(0)
	s_waitcnt vmcnt(6)
	v_mov_b32_dpp v147, v166 row_shr:2 row_mask:0xf bank_mask:0xf bound_ctrl:1
	s_waitcnt vmcnt(5)
	v_and_b32_dpp v155, v182, v157 row_ror:2 row_mask:0xf bank_mask:0xf bound_ctrl:1
	v_mov_b32_dpp v139, v166 row_shr:1 row_mask:0xf bank_mask:0xf bound_ctrl:1
	v_and_b32_dpp v153, v182, v158 row_ror:1 row_mask:0xf bank_mask:0xf bound_ctrl:1
	v_or_b32_sdwa v154, v155, v147 dst_sel:WORD_1 dst_unused:UNUSED_PAD src0_sel:DWORD src1_sel:DWORD
	v_mov_b32_dpp v156, v167 row_shr:1 row_mask:0xf bank_mask:0xf bound_ctrl:1
	v_mov_b32_dpp v171, v167 row_shr:2 row_mask:0xf bank_mask:0xf bound_ctrl:1
	v_and_b32_dpp v187, v183, v158 row_ror:1 row_mask:0xf bank_mask:0xf bound_ctrl:1
	v_and_b32_dpp v183, v183, v157 row_ror:2 row_mask:0xf bank_mask:0xf bound_ctrl:1
	v_mov_b32_dpp v189, v168 row_shr:1 row_mask:0xf bank_mask:0xf bound_ctrl:1
	v_mov_b32_dpp v191, v168 row_shr:2 row_mask:0xf bank_mask:0xf bound_ctrl:1
	v_and_b32_dpp v192, v184, v158 row_ror:1 row_mask:0xf bank_mask:0xf bound_ctrl:1
	v_and_b32_dpp v193, v184, v157 row_ror:2 row_mask:0xf bank_mask:0xf bound_ctrl:1
	v_bitop3_b32 v155, v155, s20, v147 bitop3:0xc8
	v_or_b32_sdwa v146, v153, v139 dst_sel:WORD_1 dst_unused:UNUSED_PAD src0_sel:DWORD src1_sel:DWORD
	v_or_b32_sdwa v170, v187, v156 dst_sel:WORD_1 dst_unused:UNUSED_PAD src0_sel:DWORD src1_sel:DWORD
	v_or_b32_sdwa v182, v183, v171 dst_sel:WORD_1 dst_unused:UNUSED_PAD src0_sel:DWORD src1_sel:DWORD
	v_or_b32_sdwa v186, v192, v189 dst_sel:WORD_1 dst_unused:UNUSED_PAD src0_sel:DWORD src1_sel:DWORD
	v_or_b32_sdwa v184, v193, v191 dst_sel:WORD_1 dst_unused:UNUSED_PAD src0_sel:DWORD src1_sel:DWORD
	v_and_b32_dpp v234, v185, v158 row_ror:1 row_mask:0xf bank_mask:0xf bound_ctrl:1
	v_and_b32_dpp v235, v185, v157 row_ror:2 row_mask:0xf bank_mask:0xf bound_ctrl:1
	v_bitop3_b32 v147, v153, s20, v139 bitop3:0xc8
	v_bitop3_b32 v183, v183, s20, v171 bitop3:0xc8
	v_bitop3_b32 v171, v187, s20, v156 bitop3:0xc8
	v_bitop3_b32 v185, v193, s20, v191 bitop3:0xc8
	v_bitop3_b32 v187, v192, s20, v189 bitop3:0xc8
	s_waitcnt vmcnt(4)
	v_pk_mul_f32 v[192:193], v[110:111], v[138:139] op_sel_hi:[1,0]
	v_pk_mul_f32 v[110:111], v[116:117], v[154:155]
	v_pk_mul_f32 v[114:115], v[114:115], v[138:139] op_sel_hi:[1,0]
	v_pk_fma_f32 v[110:111], v[128:129], v[146:147], v[110:111]
	v_lshlrev_b32_e32 v146, 16, v166
	v_and_b32_e32 v147, 0xffff0000, v166
	v_pk_fma_f32 v[110:111], v[120:121], v[146:147], v[110:111]
	v_pk_mul_f32 v[112:113], v[112:113], v[138:139] op_sel_hi:[1,0]
	v_pk_add_f32 v[110:111], v[124:125], v[110:111]
	v_lshlrev_b32_e32 v154, 16, v167
	v_mul_f32_e32 v139, 0xbfb8aa3b, v110
	v_exp_f32_e32 v146, v139
	v_mul_f32_e32 v139, 0xbfb8aa3b, v111
	v_exp_f32_e32 v147, v139
	v_pk_mul_f32 v[138:139], v[108:109], v[138:139] op_sel_hi:[1,0]
	v_add_f32_e32 v108, 1.0, v146
	v_and_b32_e32 v155, 0xffff0000, v167
	v_add_f32_e32 v109, 1.0, v147
	v_pk_mul_f32 v[146:147], v[118:119], v[182:183]
	v_rcp_f32_e32 v108, v108
	v_pk_fma_f32 v[146:147], v[130:131], v[170:171], v[146:147]
	v_rcp_f32_e32 v109, v109
	v_pk_fma_f32 v[146:147], v[122:123], v[154:155], v[146:147]
	v_mov_b32_dpp v233, v169 row_shr:2 row_mask:0xf bank_mask:0xf bound_ctrl:1
	v_pk_add_f32 v[146:147], v[126:127], v[146:147]
	v_pk_mul_f32 v[108:109], v[110:111], v[108:109]
	v_mul_f32_e32 v153, 0xbfb8aa3b, v146
	v_exp_f32_e32 v153, v153
	v_mul_f32_e32 v154, 0xbfb8aa3b, v147
	v_exp_f32_e32 v155, v154
	v_pk_mul_f32 v[108:109], v[108:109], v[112:113]
	v_add_f32_e32 v153, 1.0, v153
	v_rcp_f32_e32 v154, v153
	v_add_f32_e32 v153, 1.0, v155
	v_rcp_f32_e32 v155, v153
	v_pk_mul_f32 v[112:113], v[44:45], v[184:185]
	v_cvt_pk_bf16_f32 v108, v108, v109
	v_pk_fma_f32 v[112:113], v[48:49], v[186:187], v[112:113]
	v_pk_mul_f32 v[110:111], v[146:147], v[154:155]
	v_mov_b32_dpp v232, v169 row_shr:1 row_mask:0xf bank_mask:0xf bound_ctrl:1
	v_pk_mul_f32 v[110:111], v[110:111], v[114:115]
	v_lshlrev_b32_e32 v114, 16, v168
	v_and_b32_e32 v115, 0xffff0000, v168
	v_pk_fma_f32 v[112:113], v[36:37], v[114:115], v[112:113]
	v_or_b32_sdwa v190, v235, v233 dst_sel:WORD_1 dst_unused:UNUSED_PAD src0_sel:DWORD src1_sel:DWORD
	v_pk_add_f32 v[112:113], v[40:41], v[112:113]
	v_bitop3_b32 v191, v235, s20, v233 bitop3:0xc8
	v_mul_f32_e32 v109, 0xbfb8aa3b, v112
	v_exp_f32_e32 v114, v109
	v_mul_f32_e32 v109, 0xbfb8aa3b, v113
	v_exp_f32_e32 v115, v109
	v_or_b32_sdwa v188, v234, v232 dst_sel:WORD_1 dst_unused:UNUSED_PAD src0_sel:DWORD src1_sel:DWORD
	v_bitop3_b32 v189, v234, s20, v232 bitop3:0xc8
	v_cvt_pk_bf16_f32 v109, v110, v111
	v_add_f32_e32 v110, 1.0, v114
	v_add_f32_e32 v111, 1.0, v115
	v_pk_mul_f32 v[114:115], v[46:47], v[190:191]
	v_lshlrev_b32_e32 v146, 16, v169
	v_pk_fma_f32 v[114:115], v[50:51], v[188:189], v[114:115]
	v_and_b32_e32 v147, 0xffff0000, v169
	v_pk_fma_f32 v[114:115], v[38:39], v[146:147], v[114:115]
	v_rcp_f32_e32 v110, v110
	v_pk_add_f32 v[114:115], v[42:43], v[114:115]
	v_rcp_f32_e32 v111, v111
	v_mul_f32_e32 v146, 0xbfb8aa3b, v114
	v_mul_f32_e32 v147, 0xbfb8aa3b, v115
	v_exp_f32_e32 v146, v146
	v_exp_f32_e32 v147, v147
	v_pk_mul_f32 v[110:111], v[112:113], v[110:111]
	v_add_u32_e32 v156, 0xa0, v220
	v_add_f32_e32 v146, 1.0, v146
	v_add_f32_e32 v147, 1.0, v147
	v_rcp_f32_e32 v146, v146
	v_rcp_f32_e32 v147, v147
	v_pk_mul_f32 v[110:111], v[138:139], v[110:111]
	v_pk_mul_f32 v[112:113], v[114:115], v[146:147]
	s_nop 0
	v_pk_mul_f32 v[112:113], v[192:193], v[112:113]
	v_cvt_pk_bf16_f32 v110, v110, v111
	v_cvt_pk_bf16_f32 v111, v112, v113
	v_mad_i64_i32 v[112:113], s[18:19], v165, s21, v[218:219]
	v_lshl_add_u64 v[138:139], v[112:113], 0, v[206:207]
	global_store_dwordx4 v[138:139], v[108:111], off
	s_waitcnt vmcnt(4)
	v_mov_b32_e32 v112, v227
	v_sub_u32_e32 v113, v159, v1
	v_and_b32_e32 v113, 0xfdf, v113
	v_cmp_ne_u32_e32 vcc, 0, v113
	s_waitcnt vmcnt(1)
	v_mov_b32_dpp v115, v132 row_shr:2 row_mask:0xf bank_mask:0xf bound_ctrl:1
	v_mov_b32_dpp v183, v133 row_shr:1 row_mask:0xf bank_mask:0xf bound_ctrl:1
	v_cndmask_b32_e64 v113, 0, -1, vcc
	v_cndmask_b32_e64 v154, 0, v113, s[38:39]
	v_cndmask_b32_e64 v155, 0, v113, s[36:37]
	v_mov_b32_dpp v113, v132 row_shr:1 row_mask:0xf bank_mask:0xf bound_ctrl:1
	v_and_b32_dpp v147, v166, v154 row_ror:2 row_mask:0xf bank_mask:0xf bound_ctrl:1
	v_and_b32_dpp v153, v166, v155 row_ror:1 row_mask:0xf bank_mask:0xf bound_ctrl:1
	v_or_b32_sdwa v146, v147, v115 dst_sel:WORD_1 dst_unused:UNUSED_PAD src0_sel:DWORD src1_sel:DWORD
	v_mov_b32_dpp v171, v133 row_shr:2 row_mask:0xf bank_mask:0xf bound_ctrl:1
	v_and_b32_dpp v185, v167, v155 row_ror:1 row_mask:0xf bank_mask:0xf bound_ctrl:1
	v_and_b32_dpp v167, v167, v154 row_ror:2 row_mask:0xf bank_mask:0xf bound_ctrl:1
	v_mov_b32_dpp v187, v134 row_shr:1 row_mask:0xf bank_mask:0xf bound_ctrl:1
	v_mov_b32_dpp v188, v134 row_shr:2 row_mask:0xf bank_mask:0xf bound_ctrl:1
	v_and_b32_dpp v189, v168, v155 row_ror:1 row_mask:0xf bank_mask:0xf bound_ctrl:1
	v_and_b32_dpp v190, v168, v154 row_ror:2 row_mask:0xf bank_mask:0xf bound_ctrl:1
	v_bitop3_b32 v147, v147, s20, v115 bitop3:0xc8
	v_or_b32_sdwa v114, v153, v113 dst_sel:WORD_1 dst_unused:UNUSED_PAD src0_sel:DWORD src1_sel:DWORD
	v_or_b32_sdwa v166, v185, v183 dst_sel:WORD_1 dst_unused:UNUSED_PAD src0_sel:DWORD src1_sel:DWORD
	v_or_b32_sdwa v170, v167, v171 dst_sel:WORD_1 dst_unused:UNUSED_PAD src0_sel:DWORD src1_sel:DWORD
	v_or_b32_sdwa v182, v189, v187 dst_sel:WORD_1 dst_unused:UNUSED_PAD src0_sel:DWORD src1_sel:DWORD
	v_or_b32_sdwa v168, v190, v188 dst_sel:WORD_1 dst_unused:UNUSED_PAD src0_sel:DWORD src1_sel:DWORD
	v_and_b32_dpp v193, v169, v155 row_ror:1 row_mask:0xf bank_mask:0xf bound_ctrl:1
	v_and_b32_dpp v232, v169, v154 row_ror:2 row_mask:0xf bank_mask:0xf bound_ctrl:1
	v_bitop3_b32 v115, v153, s20, v113 bitop3:0xc8
	v_bitop3_b32 v171, v167, s20, v171 bitop3:0xc8
	v_bitop3_b32 v167, v185, s20, v183 bitop3:0xc8
	v_bitop3_b32 v169, v190, s20, v188 bitop3:0xc8
	v_bitop3_b32 v183, v189, s20, v187 bitop3:0xc8
	v_mov_b32_dpp v192, v135 row_shr:2 row_mask:0xf bank_mask:0xf bound_ctrl:1
	v_mov_b32_dpp v191, v135 row_shr:1 row_mask:0xf bank_mask:0xf bound_ctrl:1
	v_or_b32_sdwa v186, v232, v192 dst_sel:WORD_1 dst_unused:UNUSED_PAD src0_sel:DWORD src1_sel:DWORD
	v_bitop3_b32 v187, v232, s20, v192 bitop3:0xc8
	v_or_b32_sdwa v184, v193, v191 dst_sel:WORD_1 dst_unused:UNUSED_PAD src0_sel:DWORD src1_sel:DWORD
	v_bitop3_b32 v185, v193, s20, v191 bitop3:0xc8
	v_mad_i64_i32 v[108:109], s[18:19], v156, s21, v[224:225]
	global_load_dwordx4 v[108:111], v[108:109], off
	v_add_u32_e32 v153, 0xb0, v220
	s_waitcnt lgkmcnt(0)
	v_pk_mul_f32 v[188:189], v[102:103], v[112:113] op_sel_hi:[1,0]
	v_pk_mul_f32 v[102:103], v[116:117], v[146:147]
	v_pk_mul_f32 v[106:107], v[106:107], v[112:113] op_sel_hi:[1,0]
	v_pk_fma_f32 v[102:103], v[128:129], v[114:115], v[102:103]
	v_lshlrev_b32_e32 v114, 16, v132
	v_and_b32_e32 v115, 0xffff0000, v132
	v_pk_fma_f32 v[102:103], v[120:121], v[114:115], v[102:103]
	v_pk_mul_f32 v[104:105], v[104:105], v[112:113] op_sel_hi:[1,0]
	v_pk_add_f32 v[102:103], v[124:125], v[102:103]
	v_lshlrev_b32_e32 v146, 16, v133
	v_mul_f32_e32 v113, 0xbfb8aa3b, v102
	v_exp_f32_e32 v114, v113
	v_mul_f32_e32 v113, 0xbfb8aa3b, v103
	v_exp_f32_e32 v115, v113
	v_pk_mul_f32 v[112:113], v[100:101], v[112:113] op_sel_hi:[1,0]
	v_add_f32_e32 v100, 1.0, v114
	v_and_b32_e32 v147, 0xffff0000, v133
	v_add_f32_e32 v101, 1.0, v115
	v_pk_mul_f32 v[114:115], v[118:119], v[170:171]
	v_rcp_f32_e32 v100, v100
	v_pk_fma_f32 v[114:115], v[130:131], v[166:167], v[114:115]
	v_rcp_f32_e32 v101, v101
	v_pk_fma_f32 v[114:115], v[122:123], v[146:147], v[114:115]
	v_pk_mul_f32 v[100:101], v[102:103], v[100:101]
	v_pk_add_f32 v[114:115], v[126:127], v[114:115]
	v_pk_mul_f32 v[100:101], v[100:101], v[104:105]
	v_mul_f32_e32 v146, 0xbfb8aa3b, v114
	v_mul_f32_e32 v147, 0xbfb8aa3b, v115
	v_exp_f32_e32 v146, v146
	v_exp_f32_e32 v147, v147
	v_pk_mul_f32 v[104:105], v[44:45], v[168:169]
	v_cvt_pk_bf16_f32 v100, v100, v101
	v_add_f32_e32 v146, 1.0, v146
	v_add_f32_e32 v147, 1.0, v147
	v_rcp_f32_e32 v146, v146
	v_rcp_f32_e32 v147, v147
	v_pk_fma_f32 v[104:105], v[48:49], v[182:183], v[104:105]
	v_pk_mul_f32 v[102:103], v[114:115], v[146:147]
	s_nop 0
	v_pk_mul_f32 v[102:103], v[102:103], v[106:107]
	v_lshlrev_b32_e32 v106, 16, v134
	v_and_b32_e32 v107, 0xffff0000, v134
	v_pk_fma_f32 v[104:105], v[36:37], v[106:107], v[104:105]
	v_lshlrev_b32_e32 v114, 16, v135
	v_pk_add_f32 v[104:105], v[40:41], v[104:105]
	v_and_b32_e32 v115, 0xffff0000, v135
	v_mul_f32_e32 v101, 0xbfb8aa3b, v104
	v_exp_f32_e32 v106, v101
	v_mul_f32_e32 v101, 0xbfb8aa3b, v105
	v_exp_f32_e32 v107, v101
	v_cvt_pk_bf16_f32 v101, v102, v103
	v_add_f32_e32 v102, 1.0, v106
	v_rcp_f32_e32 v102, v102
	v_add_f32_e32 v103, 1.0, v107
	v_pk_mul_f32 v[106:107], v[46:47], v[186:187]
	v_rcp_f32_e32 v103, v103
	v_pk_fma_f32 v[106:107], v[50:51], v[184:185], v[106:107]
	v_pk_mul_f32 v[102:103], v[104:105], v[102:103]
	v_pk_fma_f32 v[106:107], v[38:39], v[114:115], v[106:107]
	v_pk_mul_f32 v[102:103], v[112:113], v[102:103]
	v_pk_add_f32 v[106:107], v[42:43], v[106:107]
	v_cvt_pk_bf16_f32 v102, v102, v103
	v_mul_f32_e32 v114, 0xbfb8aa3b, v106
	v_mul_f32_e32 v115, 0xbfb8aa3b, v107
	v_exp_f32_e32 v114, v114
	v_exp_f32_e32 v115, v115
	v_add_f32_e32 v114, 1.0, v114
	v_add_f32_e32 v115, 1.0, v115
	v_rcp_f32_e32 v114, v114
	v_rcp_f32_e32 v115, v115
	s_nop 0
	v_pk_mul_f32 v[104:105], v[106:107], v[114:115]
	s_nop 0
	v_pk_mul_f32 v[104:105], v[188:189], v[104:105]
	s_nop 0
	v_cvt_pk_bf16_f32 v103, v104, v105
	v_mad_i64_i32 v[104:105], s[18:19], v159, s21, v[218:219]
	v_lshl_add_u64 v[114:115], v[104:105], 0, v[206:207]
	global_store_dwordx4 v[114:115], v[100:103], off
	s_nop 1
	v_mov_b32_e32 v100, v228
	s_nop 0
	v_sub_u32_e32 v101, v156, v1
	v_and_b32_e32 v101, 0xfff, v101
	v_cmp_ne_u32_e32 vcc, 0, v101
	v_mad_i64_i32 v[102:103], s[18:19], v153, s21, v[224:225]
	s_nop 0
	v_cndmask_b32_e64 v101, 0, -1, vcc
	v_cndmask_b32_e64 v146, 0, v101, s[38:39]
	global_load_dwordx4 v[102:105], v[102:103], off
	v_cndmask_b32_e64 v147, 0, v101, s[36:37]
	s_waitcnt vmcnt(2)
	v_mov_b32_dpp v107, v108 row_shr:2 row_mask:0xf bank_mask:0xf bound_ctrl:1
	v_and_b32_dpp v113, v132, v146 row_ror:2 row_mask:0xf bank_mask:0xf bound_ctrl:1
	v_mov_b32_dpp v101, v108 row_shr:1 row_mask:0xf bank_mask:0xf bound_ctrl:1
	v_and_b32_dpp v167, v132, v147 row_ror:1 row_mask:0xf bank_mask:0xf bound_ctrl:1
	v_or_b32_sdwa v112, v113, v107 dst_sel:WORD_1 dst_unused:UNUSED_PAD src0_sel:DWORD src1_sel:DWORD
	v_mov_b32_dpp v169, v109 row_shr:1 row_mask:0xf bank_mask:0xf bound_ctrl:1
	v_mov_b32_dpp v171, v109 row_shr:2 row_mask:0xf bank_mask:0xf bound_ctrl:1
	v_and_b32_dpp v183, v133, v147 row_ror:1 row_mask:0xf bank_mask:0xf bound_ctrl:1
	v_and_b32_dpp v133, v133, v146 row_ror:2 row_mask:0xf bank_mask:0xf bound_ctrl:1
	v_mov_b32_dpp v184, v110 row_shr:1 row_mask:0xf bank_mask:0xf bound_ctrl:1
	v_mov_b32_dpp v185, v110 row_shr:2 row_mask:0xf bank_mask:0xf bound_ctrl:1
	v_and_b32_dpp v186, v134, v147 row_ror:1 row_mask:0xf bank_mask:0xf bound_ctrl:1
	v_and_b32_dpp v187, v134, v146 row_ror:2 row_mask:0xf bank_mask:0xf bound_ctrl:1
	v_bitop3_b32 v113, v113, s20, v107 bitop3:0xc8
	v_or_b32_sdwa v106, v167, v101 dst_sel:WORD_1 dst_unused:UNUSED_PAD src0_sel:DWORD src1_sel:DWORD
	v_or_b32_sdwa v132, v183, v169 dst_sel:WORD_1 dst_unused:UNUSED_PAD src0_sel:DWORD src1_sel:DWORD
	v_or_b32_sdwa v166, v133, v171 dst_sel:WORD_1 dst_unused:UNUSED_PAD src0_sel:DWORD src1_sel:DWORD
	v_or_b32_sdwa v168, v186, v184 dst_sel:WORD_1 dst_unused:UNUSED_PAD src0_sel:DWORD src1_sel:DWORD
	v_or_b32_sdwa v134, v187, v185 dst_sel:WORD_1 dst_unused:UNUSED_PAD src0_sel:DWORD src1_sel:DWORD
	v_and_b32_dpp v190, v135, v147 row_ror:1 row_mask:0xf bank_mask:0xf bound_ctrl:1
	v_and_b32_dpp v191, v135, v146 row_ror:2 row_mask:0xf bank_mask:0xf bound_ctrl:1
	v_bitop3_b32 v107, v167, s20, v101 bitop3:0xc8
	v_bitop3_b32 v167, v133, s20, v171 bitop3:0xc8
	v_bitop3_b32 v133, v183, s20, v169 bitop3:0xc8
	v_bitop3_b32 v135, v187, s20, v185 bitop3:0xc8
	v_bitop3_b32 v169, v186, s20, v184 bitop3:0xc8
	v_mov_b32_dpp v189, v111 row_shr:2 row_mask:0xf bank_mask:0xf bound_ctrl:1
	v_mov_b32_dpp v188, v111 row_shr:1 row_mask:0xf bank_mask:0xf bound_ctrl:1
	v_or_b32_sdwa v182, v191, v189 dst_sel:WORD_1 dst_unused:UNUSED_PAD src0_sel:DWORD src1_sel:DWORD
	v_bitop3_b32 v183, v191, s20, v189 bitop3:0xc8
	v_or_b32_sdwa v170, v190, v188 dst_sel:WORD_1 dst_unused:UNUSED_PAD src0_sel:DWORD src1_sel:DWORD
	v_bitop3_b32 v171, v190, s20, v188 bitop3:0xc8
	s_andn2_b64 vcc, exec, s[40:41]
	s_waitcnt lgkmcnt(0)
	v_pk_mul_f32 v[184:185], v[62:63], v[100:101] op_sel_hi:[1,0]
	v_pk_mul_f32 v[62:63], v[116:117], v[112:113]
	v_pk_mul_f32 v[66:67], v[66:67], v[100:101] op_sel_hi:[1,0]
	v_pk_fma_f32 v[62:63], v[128:129], v[106:107], v[62:63]
	v_lshlrev_b32_e32 v106, 16, v108
	v_and_b32_e32 v107, 0xffff0000, v108
	v_pk_fma_f32 v[62:63], v[120:121], v[106:107], v[62:63]
	v_pk_mul_f32 v[64:65], v[64:65], v[100:101] op_sel_hi:[1,0]
	v_pk_add_f32 v[62:63], v[124:125], v[62:63]
	v_lshlrev_b32_e32 v112, 16, v109
	v_mul_f32_e32 v101, 0xbfb8aa3b, v62
	v_exp_f32_e32 v106, v101
	v_mul_f32_e32 v101, 0xbfb8aa3b, v63
	v_exp_f32_e32 v107, v101
	v_pk_mul_f32 v[100:101], v[60:61], v[100:101] op_sel_hi:[1,0]
	v_add_f32_e32 v60, 1.0, v106
	v_and_b32_e32 v113, 0xffff0000, v109
	v_add_f32_e32 v61, 1.0, v107
	v_pk_mul_f32 v[106:107], v[118:119], v[166:167]
	v_rcp_f32_e32 v60, v60
	v_pk_fma_f32 v[106:107], v[130:131], v[132:133], v[106:107]
	v_rcp_f32_e32 v61, v61
	v_pk_fma_f32 v[106:107], v[122:123], v[112:113], v[106:107]
	s_waitcnt vmcnt(0)
	v_mov_b32_dpp v133, v103 row_shr:2 row_mask:0xf bank_mask:0xf bound_ctrl:1
	v_pk_add_f32 v[106:107], v[126:127], v[106:107]
	v_pk_mul_f32 v[60:61], v[62:63], v[60:61]
	v_mul_f32_e32 v112, 0xbfb8aa3b, v106
	v_mul_f32_e32 v113, 0xbfb8aa3b, v107
	v_exp_f32_e32 v112, v112
	v_exp_f32_e32 v113, v113
	v_pk_mul_f32 v[60:61], v[60:61], v[64:65]
	v_pk_mul_f32 v[64:65], v[44:45], v[134:135]
	v_add_f32_e32 v112, 1.0, v112
	v_add_f32_e32 v113, 1.0, v113
	v_rcp_f32_e32 v112, v112
	v_rcp_f32_e32 v113, v113
	v_pk_fma_f32 v[64:65], v[48:49], v[168:169], v[64:65]
	v_cvt_pk_bf16_f32 v60, v60, v61
	v_mov_b32_dpp v135, v104 row_shr:1 row_mask:0xf bank_mask:0xf bound_ctrl:1
	v_pk_mul_f32 v[62:63], v[106:107], v[112:113]
	v_lshlrev_b32_e32 v106, 16, v111
	v_pk_mul_f32 v[62:63], v[62:63], v[66:67]
	v_lshlrev_b32_e32 v66, 16, v110
	v_and_b32_e32 v67, 0xffff0000, v110
	v_pk_fma_f32 v[64:65], v[36:37], v[66:67], v[64:65]
	v_and_b32_e32 v107, 0xffff0000, v111
	v_pk_add_f32 v[64:65], v[40:41], v[64:65]
	v_mov_b32_dpp v166, v104 row_shr:2 row_mask:0xf bank_mask:0xf bound_ctrl:1
	v_mul_f32_e32 v61, 0xbfb8aa3b, v64
	v_exp_f32_e32 v66, v61
	v_mul_f32_e32 v61, 0xbfb8aa3b, v65
	v_exp_f32_e32 v67, v61
	v_cvt_pk_bf16_f32 v61, v62, v63
	v_add_f32_e32 v62, 1.0, v66
	v_rcp_f32_e32 v62, v62
	v_add_f32_e32 v63, 1.0, v67
	v_pk_mul_f32 v[66:67], v[46:47], v[182:183]
	v_rcp_f32_e32 v63, v63
	v_pk_fma_f32 v[66:67], v[50:51], v[170:171], v[66:67]
	v_mov_b32_dpp v170, v105 row_shr:2 row_mask:0xf bank_mask:0xf bound_ctrl:1
	v_pk_fma_f32 v[66:67], v[38:39], v[106:107], v[66:67]
	v_pk_mul_f32 v[62:63], v[64:65], v[62:63]
	v_pk_add_f32 v[66:67], v[42:43], v[66:67]
	v_pk_mul_f32 v[62:63], v[100:101], v[62:63]
	v_mul_f32_e32 v106, 0xbfb8aa3b, v66
	v_mul_f32_e32 v107, 0xbfb8aa3b, v67
	v_exp_f32_e32 v106, v106
	v_exp_f32_e32 v107, v107
	v_cvt_pk_bf16_f32 v62, v62, v63
	v_mov_b32_dpp v169, v105 row_shr:1 row_mask:0xf bank_mask:0xf bound_ctrl:1
	v_add_f32_e32 v106, 1.0, v106
	v_add_f32_e32 v107, 1.0, v107
	v_rcp_f32_e32 v106, v106
	v_rcp_f32_e32 v107, v107
	s_nop 0
	v_pk_mul_f32 v[64:65], v[66:67], v[106:107]
	s_nop 0
	v_pk_mul_f32 v[64:65], v[184:185], v[64:65]
	v_mov_b32_dpp v107, v103 row_shr:1 row_mask:0xf bank_mask:0xf bound_ctrl:1
	v_cvt_pk_bf16_f32 v63, v64, v65
	v_mad_i64_i32 v[64:65], s[18:19], v156, s21, v[218:219]
	v_lshl_add_u64 v[112:113], v[64:65], 0, v[206:207]
	global_store_dwordx4 v[112:113], v[60:63], off
	v_mov_b32_e32 v64, v229
	s_nop 0
	v_mov_b32_dpp v60, v108 row_ror:1 row_mask:0xf bank_mask:0xf bound_ctrl:1
	v_mov_b32_dpp v62, v108 row_ror:2 row_mask:0xf bank_mask:0xf bound_ctrl:1
	v_cndmask_b32_e64 v65, 0, v60, s[36:37]
	v_mov_b32_dpp v60, v109 row_ror:1 row_mask:0xf bank_mask:0xf bound_ctrl:1
	v_mov_b32_dpp v63, v102 row_shr:2 row_mask:0xf bank_mask:0xf bound_ctrl:1
	v_cndmask_b32_e64 v67, 0, v62, s[38:39]
	v_mov_b32_dpp v62, v109 row_ror:2 row_mask:0xf bank_mask:0xf bound_ctrl:1
	v_cndmask_b32_e64 v134, 0, v60, s[36:37]
	v_mov_b32_dpp v60, v110 row_ror:1 row_mask:0xf bank_mask:0xf bound_ctrl:1
	v_mov_b32_dpp v61, v102 row_shr:1 row_mask:0xf bank_mask:0xf bound_ctrl:1
	v_or_b32_sdwa v100, v67, v63 dst_sel:WORD_1 dst_unused:UNUSED_PAD src0_sel:DWORD src1_sel:DWORD
	v_cndmask_b32_e64 v109, 0, v62, s[38:39]
	v_mov_b32_dpp v62, v110 row_ror:2 row_mask:0xf bank_mask:0xf bound_ctrl:1
	v_cndmask_b32_e64 v167, 0, v60, s[36:37]
	v_bitop3_b32 v101, v67, s20, v63 bitop3:0xc8
	v_or_b32_sdwa v66, v65, v61 dst_sel:WORD_1 dst_unused:UNUSED_PAD src0_sel:DWORD src1_sel:DWORD
	v_or_b32_sdwa v106, v134, v107 dst_sel:WORD_1 dst_unused:UNUSED_PAD src0_sel:DWORD src1_sel:DWORD
	v_or_b32_sdwa v110, v167, v135 dst_sel:WORD_1 dst_unused:UNUSED_PAD src0_sel:DWORD src1_sel:DWORD
	v_cndmask_b32_e64 v168, 0, v62, s[38:39]
	v_mov_b32_dpp v60, v111 row_ror:1 row_mask:0xf bank_mask:0xf bound_ctrl:1
	v_mov_b32_dpp v62, v111 row_ror:2 row_mask:0xf bank_mask:0xf bound_ctrl:1
	v_bitop3_b32 v67, v65, s20, v61 bitop3:0xc8
	v_bitop3_b32 v107, v134, s20, v107 bitop3:0xc8
	v_bitop3_b32 v111, v167, s20, v135 bitop3:0xc8
	v_or_b32_sdwa v108, v109, v133 dst_sel:WORD_1 dst_unused:UNUSED_PAD src0_sel:DWORD src1_sel:DWORD
	v_bitop3_b32 v109, v109, s20, v133 bitop3:0xc8
	v_or_b32_sdwa v132, v168, v166 dst_sel:WORD_1 dst_unused:UNUSED_PAD src0_sel:DWORD src1_sel:DWORD
	v_bitop3_b32 v133, v168, s20, v166 bitop3:0xc8
	v_pk_mul_f32 v[44:45], v[44:45], v[132:133]
	v_cndmask_b32_e64 v182, 0, v62, s[38:39]
	v_pk_fma_f32 v[44:45], v[48:49], v[110:111], v[44:45]
	v_lshlrev_b32_e32 v48, 16, v104
	v_and_b32_e32 v49, 0xffff0000, v104
	v_pk_fma_f32 v[36:37], v[36:37], v[48:49], v[44:45]
	v_cndmask_b32_e64 v171, 0, v60, s[36:37]
	v_pk_add_f32 v[40:41], v[40:41], v[36:37]
	v_or_b32_sdwa v62, v182, v170 dst_sel:WORD_1 dst_unused:UNUSED_PAD src0_sel:DWORD src1_sel:DWORD
	v_mul_f32_e32 v36, 0xbfb8aa3b, v40
	v_exp_f32_e32 v44, v36
	v_or_b32_e32 v36, 0x80, v222
	v_ashrrev_i32_e32 v37, 31, v36
	v_bitop3_b32 v63, v182, s20, v170 bitop3:0xc8
	v_mad_i64_i32 v[48:49], s[18:19], v220, s21, v[204:205]
	v_or_b32_sdwa v60, v171, v169 dst_sel:WORD_1 dst_unused:UNUSED_PAD src0_sel:DWORD src1_sel:DWORD
	v_bitop3_b32 v61, v171, s20, v169 bitop3:0xc8
	v_pk_mul_f32 v[46:47], v[46:47], v[62:63]
	v_mul_f32_e32 v45, 0xbfb8aa3b, v41
	v_pk_fma_f32 v[46:47], v[50:51], v[60:61], v[46:47]
	v_exp_f32_e32 v45, v45
	v_add_f32_e32 v44, 1.0, v44
	v_rcp_f32_e32 v44, v44
	v_add_f32_e32 v45, 1.0, v45
	v_rcp_f32_e32 v45, v45
	s_waitcnt lgkmcnt(0)
	v_pk_mul_f32 v[134:135], v[56:57], v[64:65] op_sel_hi:[1,0]
	v_pk_mul_f32 v[56:57], v[54:55], v[64:65] op_sel_hi:[1,0]
	v_pk_mul_f32 v[54:55], v[116:117], v[100:101]
	v_pk_mul_f32 v[58:59], v[58:59], v[64:65] op_sel_hi:[1,0]
	v_pk_fma_f32 v[54:55], v[128:129], v[66:67], v[54:55]
	v_lshlrev_b32_e32 v66, 16, v102
	v_and_b32_e32 v67, 0xffff0000, v102
	v_pk_fma_f32 v[54:55], v[120:121], v[66:67], v[54:55]
	v_and_b32_e32 v101, 0xffff0000, v103
	v_pk_add_f32 v[66:67], v[124:125], v[54:55]
	v_pk_mul_f32 v[40:41], v[40:41], v[44:45]
	v_mul_f32_e32 v54, 0xbfb8aa3b, v66
	v_exp_f32_e32 v65, v54
	v_mul_f32_e32 v54, 0xbfb8aa3b, v67
	v_exp_f32_e32 v100, v54
	v_pk_mul_f32 v[54:55], v[52:53], v[64:65] op_sel_hi:[1,0]
	v_add_f32_e32 v52, 1.0, v65
	v_pk_mul_f32 v[64:65], v[118:119], v[108:109]
	v_add_f32_e32 v53, 1.0, v100
	v_pk_fma_f32 v[64:65], v[130:131], v[106:107], v[64:65]
	v_lshlrev_b32_e32 v100, 16, v103
	v_pk_fma_f32 v[64:65], v[122:123], v[100:101], v[64:65]
	v_lshlrev_b64 v[108:109], 1, v[36:37]
	v_pk_add_f32 v[64:65], v[126:127], v[64:65]
	v_lshl_add_u64 v[48:49], v[48:49], 0, v[108:109]
	v_mul_f32_e32 v100, 0xbfb8aa3b, v64
	v_mul_f32_e32 v101, 0xbfb8aa3b, v65
	v_exp_f32_e32 v100, v100
	v_exp_f32_e32 v101, v101
	global_load_dwordx4 v[116:119], v[216:217], off offset:256
	v_rcp_f32_e32 v52, v52
	v_add_f32_e32 v100, 1.0, v100
	v_add_f32_e32 v101, 1.0, v101
	v_rcp_f32_e32 v100, v100
	v_rcp_f32_e32 v101, v101
	v_rcp_f32_e32 v53, v53
	v_pk_mul_f32 v[40:41], v[54:55], v[40:41]
	v_lshlrev_b64 v[36:37], 2, v[36:37]
	v_pk_mul_f32 v[64:65], v[64:65], v[100:101]
	global_load_dwordx4 v[100:103], v[48:49], off
	v_lshlrev_b32_e32 v48, 16, v105
	v_and_b32_e32 v49, 0xffff0000, v105
	v_pk_fma_f32 v[38:39], v[38:39], v[48:49], v[46:47]
	v_pk_mul_f32 v[52:53], v[66:67], v[52:53]
	v_pk_add_f32 v[38:39], v[42:43], v[38:39]
	v_pk_mul_f32 v[52:53], v[52:53], v[134:135]
	v_mul_f32_e32 v42, 0xbfb8aa3b, v38
	v_mul_f32_e32 v43, 0xbfb8aa3b, v39
	v_exp_f32_e32 v42, v42
	v_exp_f32_e32 v43, v43
	v_pk_mul_f32 v[58:59], v[64:65], v[58:59]
	v_cvt_pk_bf16_f32 v52, v52, v53
	v_add_f32_e32 v42, 1.0, v42
	v_add_f32_e32 v43, 1.0, v43
	v_rcp_f32_e32 v42, v42
	v_rcp_f32_e32 v43, v43
	v_cvt_pk_bf16_f32 v53, v58, v59
	v_cvt_pk_bf16_f32 v54, v40, v41
	v_mad_i64_i32 v[104:105], s[18:19], v212, s21, v[204:205]
	v_pk_mul_f32 v[38:39], v[38:39], v[42:43]
	v_lshl_add_u64 v[104:105], v[104:105], 0, v[108:109]
	v_pk_mul_f32 v[38:39], v[56:57], v[38:39]
	s_waitcnt lgkmcnt(0)
	s_waitcnt vmcnt(1)
	v_and_b32_dpp v127, v116, v223 row_ror:2 row_mask:0xf bank_mask:0xf bound_ctrl:1
	v_cvt_pk_bf16_f32 v55, v38, v39
	v_mad_i64_i32 v[38:39], s[18:19], v153, s21, v[218:219]
	v_lshl_add_u64 v[110:111], v[38:39], 0, v[206:207]
	global_store_dwordx4 v[110:111], v[52:55], off
	global_load_dword v120, v[202:203], off
	global_load_dword v227, v[202:203], off offset:64
	global_load_dword v228, v[202:203], off offset:128
	global_load_dword v229, v[202:203], off offset:192
	v_lshl_add_u64 v[38:39], v[194:195], 0, v[36:37]
	global_load_dwordx4 v[64:67], v[208:209], off offset:512
	global_load_dwordx4 v[60:63], v[38:39], off
	v_lshl_add_u64 v[36:37], v[196:197], 0, v[36:37]
	global_load_dwordx4 v[52:55], v[36:37], off
	global_load_dwordx4 v[56:59], v[210:211], off offset:512
	global_load_dwordx4 v[48:51], v[208:209], off offset:528
	global_load_dwordx4 v[44:47], v[38:39], off offset:16
	s_nop 0
	global_load_dwordx4 v[36:39], v[36:37], off offset:16
	s_nop 0
	global_load_dwordx4 v[40:43], v[210:211], off offset:528
	s_waitcnt vmcnt(13)
	v_mov_b32_dpp v123, v100 row_shr:2 row_mask:0xf bank_mask:0xf bound_ctrl:1
	v_mov_b32_dpp v121, v100 row_shr:1 row_mask:0xf bank_mask:0xf bound_ctrl:1
	v_and_b32_dpp v125, v116, v245 row_ror:1 row_mask:0xf bank_mask:0xf bound_ctrl:1
	v_or_b32_sdwa v116, v127, v123 dst_sel:WORD_1 dst_unused:UNUSED_PAD src0_sel:DWORD src1_sel:DWORD
	v_mov_b32_dpp v129, v101 row_shr:1 row_mask:0xf bank_mask:0xf bound_ctrl:1
	v_mov_b32_dpp v131, v101 row_shr:2 row_mask:0xf bank_mask:0xf bound_ctrl:1
	v_and_b32_dpp v133, v117, v245 row_ror:1 row_mask:0xf bank_mask:0xf bound_ctrl:1
	v_and_b32_dpp v134, v117, v223 row_ror:2 row_mask:0xf bank_mask:0xf bound_ctrl:1
	v_mov_b32_dpp v135, v102 row_shr:1 row_mask:0xf bank_mask:0xf bound_ctrl:1
	v_and_b32_dpp v167, v118, v245 row_ror:1 row_mask:0xf bank_mask:0xf bound_ctrl:1
	v_bitop3_b32 v117, v127, s20, v123 bitop3:0xc8
	v_or_b32_sdwa v122, v125, v121 dst_sel:WORD_1 dst_unused:UNUSED_PAD src0_sel:DWORD src1_sel:DWORD
	v_or_b32_sdwa v124, v133, v129 dst_sel:WORD_1 dst_unused:UNUSED_PAD src0_sel:DWORD src1_sel:DWORD
	v_or_b32_sdwa v126, v134, v131 dst_sel:WORD_1 dst_unused:UNUSED_PAD src0_sel:DWORD src1_sel:DWORD
	v_or_b32_sdwa v128, v167, v135 dst_sel:WORD_1 dst_unused:UNUSED_PAD src0_sel:DWORD src1_sel:DWORD
	v_bitop3_b32 v123, v125, s20, v121 bitop3:0xc8
	v_bitop3_b32 v127, v134, s20, v131 bitop3:0xc8
	v_bitop3_b32 v125, v133, s20, v129 bitop3:0xc8
	v_bitop3_b32 v129, v167, s20, v135 bitop3:0xc8
	v_mov_b32_dpp v166, v102 row_shr:2 row_mask:0xf bank_mask:0xf bound_ctrl:1
	v_and_b32_dpp v168, v118, v223 row_ror:2 row_mask:0xf bank_mask:0xf bound_ctrl:1
	v_or_b32_sdwa v118, v168, v166 dst_sel:WORD_1 dst_unused:UNUSED_PAD src0_sel:DWORD src1_sel:DWORD
	v_and_b32_dpp v171, v119, v245 row_ror:1 row_mask:0xf bank_mask:0xf bound_ctrl:1
	v_and_b32_dpp v182, v119, v223 row_ror:2 row_mask:0xf bank_mask:0xf bound_ctrl:1
	v_bitop3_b32 v119, v168, s20, v166 bitop3:0xc8
	v_mov_b32_dpp v170, v103 row_shr:2 row_mask:0xf bank_mask:0xf bound_ctrl:1
	v_mov_b32_dpp v169, v103 row_shr:1 row_mask:0xf bank_mask:0xf bound_ctrl:1
	v_or_b32_sdwa v132, v182, v170 dst_sel:WORD_1 dst_unused:UNUSED_PAD src0_sel:DWORD src1_sel:DWORD
	v_bitop3_b32 v133, v182, s20, v170 bitop3:0xc8
	v_or_b32_sdwa v130, v171, v169 dst_sel:WORD_1 dst_unused:UNUSED_PAD src0_sel:DWORD src1_sel:DWORD
	v_bitop3_b32 v131, v171, s20, v169 bitop3:0xc8
	global_load_dwordx4 v[104:107], v[104:105], off
	s_waitcnt lgkmcnt(0)
	s_waitcnt vmcnt(12)
	v_pk_mul_f32 v[134:135], v[94:95], v[120:121] op_sel_hi:[1,0]
	s_waitcnt vmcnt(8)
	v_pk_mul_f32 v[94:95], v[64:65], v[116:117]
	v_lshlrev_b32_e32 v116, 16, v100
	s_waitcnt vmcnt(7)
	v_pk_fma_f32 v[94:95], v[60:61], v[122:123], v[94:95]
	v_and_b32_e32 v117, 0xffff0000, v100
	s_waitcnt vmcnt(6)
	v_pk_fma_f32 v[94:95], v[52:53], v[116:117], v[94:95]
	v_pk_mul_f32 v[98:99], v[98:99], v[120:121] op_sel_hi:[1,0]
	s_waitcnt vmcnt(5)
	v_pk_add_f32 v[94:95], v[56:57], v[94:95]
	v_pk_mul_f32 v[96:97], v[96:97], v[120:121] op_sel_hi:[1,0]
	v_mul_f32_e32 v116, 0xbfb8aa3b, v94
	v_exp_f32_e32 v121, v116
	v_mul_f32_e32 v116, 0xbfb8aa3b, v95
	v_exp_f32_e32 v122, v116
	v_and_b32_e32 v123, 0xffff0000, v101
	v_pk_mul_f32 v[116:117], v[92:93], v[120:121] op_sel_hi:[1,0]
	v_add_f32_e32 v92, 1.0, v121
	v_pk_mul_f32 v[120:121], v[66:67], v[126:127]
	v_add_f32_e32 v93, 1.0, v122
	v_pk_fma_f32 v[120:121], v[62:63], v[124:125], v[120:121]
	v_lshlrev_b32_e32 v122, 16, v101
	v_pk_fma_f32 v[120:121], v[54:55], v[122:123], v[120:121]
	v_rcp_f32_e32 v92, v92
	v_pk_add_f32 v[120:121], v[58:59], v[120:121]
	v_rcp_f32_e32 v93, v93
	v_mul_f32_e32 v122, 0xbfb8aa3b, v120
	v_mul_f32_e32 v123, 0xbfb8aa3b, v121
	v_exp_f32_e32 v122, v122
	v_exp_f32_e32 v123, v123
	v_pk_mul_f32 v[92:93], v[94:95], v[92:93]
	v_and_b32_dpp v125, v101, v221 row_ror:1 row_mask:0xf bank_mask:0xf bound_ctrl:1
	v_add_f32_e32 v122, 1.0, v122
	v_add_f32_e32 v123, 1.0, v123
	v_rcp_f32_e32 v122, v122
	v_rcp_f32_e32 v123, v123
	v_pk_mul_f32 v[92:93], v[92:93], v[96:97]
	s_waitcnt vmcnt(4)
	v_pk_mul_f32 v[96:97], v[48:49], v[118:119]
	v_cvt_pk_bf16_f32 v92, v92, v93
	v_pk_mul_f32 v[94:95], v[120:121], v[122:123]
	s_waitcnt vmcnt(3)
	v_pk_fma_f32 v[96:97], v[44:45], v[128:129], v[96:97]
	v_pk_mul_f32 v[94:95], v[98:99], v[94:95]
	v_lshlrev_b32_e32 v98, 16, v102
	v_and_b32_e32 v99, 0xffff0000, v102
	s_waitcnt vmcnt(2)
	v_pk_fma_f32 v[96:97], v[36:37], v[98:99], v[96:97]
	v_lshlrev_b32_e32 v118, 16, v103
	s_waitcnt vmcnt(1)
	v_pk_add_f32 v[96:97], v[40:41], v[96:97]
	v_and_b32_e32 v119, 0xffff0000, v103
	v_mul_f32_e32 v93, 0xbfb8aa3b, v96
	v_exp_f32_e32 v98, v93
	v_mul_f32_e32 v93, 0xbfb8aa3b, v97
	v_exp_f32_e32 v99, v93
	v_cvt_pk_bf16_f32 v93, v94, v95
	v_add_f32_e32 v94, 1.0, v98
	v_rcp_f32_e32 v94, v94
	v_add_f32_e32 v95, 1.0, v99
	v_pk_mul_f32 v[98:99], v[50:51], v[132:133]
	v_rcp_f32_e32 v95, v95
	v_pk_fma_f32 v[98:99], v[46:47], v[130:131], v[98:99]
	v_and_b32_dpp v126, v101, v213 row_ror:2 row_mask:0xf bank_mask:0xf bound_ctrl:1
	v_pk_fma_f32 v[98:99], v[38:39], v[118:119], v[98:99]
	v_pk_mul_f32 v[94:95], v[96:97], v[94:95]
	v_pk_add_f32 v[98:99], v[42:43], v[98:99]
	v_pk_mul_f32 v[94:95], v[116:117], v[94:95]
	v_mul_f32_e32 v118, 0xbfb8aa3b, v98
	v_mul_f32_e32 v119, 0xbfb8aa3b, v99
	v_exp_f32_e32 v118, v118
	v_exp_f32_e32 v119, v119
	v_cvt_pk_bf16_f32 v94, v94, v95
	v_and_b32_dpp v117, v100, v221 row_ror:1 row_mask:0xf bank_mask:0xf bound_ctrl:1
	v_add_f32_e32 v118, 1.0, v118
	v_add_f32_e32 v119, 1.0, v119
	v_rcp_f32_e32 v118, v118
	v_rcp_f32_e32 v119, v119
	v_and_b32_dpp v129, v102, v221 row_ror:1 row_mask:0xf bank_mask:0xf bound_ctrl:1
	v_and_b32_dpp v130, v102, v213 row_ror:2 row_mask:0xf bank_mask:0xf bound_ctrl:1
	v_and_b32_dpp v133, v103, v221 row_ror:1 row_mask:0xf bank_mask:0xf bound_ctrl:1
	v_pk_mul_f32 v[96:97], v[98:99], v[118:119]
	v_and_b32_dpp v119, v100, v213 row_ror:2 row_mask:0xf bank_mask:0xf bound_ctrl:1
	v_pk_mul_f32 v[96:97], v[134:135], v[96:97]
	v_and_b32_dpp v134, v103, v213 row_ror:2 row_mask:0xf bank_mask:0xf bound_ctrl:1
	v_cvt_pk_bf16_f32 v95, v96, v97
	global_store_dwordx4 v[162:163], v[92:95], off offset:256
	s_nop 1
	v_mov_b32_e32 v92, v227
	s_waitcnt vmcnt(1)
	v_mov_b32_dpp v99, v104 row_shr:2 row_mask:0xf bank_mask:0xf bound_ctrl:1
	v_mov_b32_dpp v93, v104 row_shr:1 row_mask:0xf bank_mask:0xf bound_ctrl:1
	v_or_b32_sdwa v100, v119, v99 dst_sel:WORD_1 dst_unused:UNUSED_PAD src0_sel:DWORD src1_sel:DWORD
	v_mov_b32_dpp v121, v105 row_shr:1 row_mask:0xf bank_mask:0xf bound_ctrl:1
	v_mov_b32_dpp v123, v105 row_shr:2 row_mask:0xf bank_mask:0xf bound_ctrl:1
	v_mov_b32_dpp v127, v106 row_shr:1 row_mask:0xf bank_mask:0xf bound_ctrl:1
	v_bitop3_b32 v101, v119, s20, v99 bitop3:0xc8
	v_or_b32_sdwa v98, v117, v93 dst_sel:WORD_1 dst_unused:UNUSED_PAD src0_sel:DWORD src1_sel:DWORD
	v_or_b32_sdwa v116, v125, v121 dst_sel:WORD_1 dst_unused:UNUSED_PAD src0_sel:DWORD src1_sel:DWORD
	v_or_b32_sdwa v118, v126, v123 dst_sel:WORD_1 dst_unused:UNUSED_PAD src0_sel:DWORD src1_sel:DWORD
	v_or_b32_sdwa v120, v129, v127 dst_sel:WORD_1 dst_unused:UNUSED_PAD src0_sel:DWORD src1_sel:DWORD
	v_bitop3_b32 v99, v117, s20, v93 bitop3:0xc8
	v_bitop3_b32 v119, v126, s20, v123 bitop3:0xc8
	v_bitop3_b32 v117, v125, s20, v121 bitop3:0xc8
	v_bitop3_b32 v121, v129, s20, v127 bitop3:0xc8
	v_mov_b32_dpp v128, v106 row_shr:2 row_mask:0xf bank_mask:0xf bound_ctrl:1
	v_or_b32_sdwa v102, v130, v128 dst_sel:WORD_1 dst_unused:UNUSED_PAD src0_sel:DWORD src1_sel:DWORD
	v_bitop3_b32 v103, v130, s20, v128 bitop3:0xc8
	v_mov_b32_dpp v132, v107 row_shr:2 row_mask:0xf bank_mask:0xf bound_ctrl:1
	v_mov_b32_dpp v131, v107 row_shr:1 row_mask:0xf bank_mask:0xf bound_ctrl:1
	v_or_b32_sdwa v124, v134, v132 dst_sel:WORD_1 dst_unused:UNUSED_PAD src0_sel:DWORD src1_sel:DWORD
	v_bitop3_b32 v125, v134, s20, v132 bitop3:0xc8
	v_or_b32_sdwa v122, v133, v131 dst_sel:WORD_1 dst_unused:UNUSED_PAD src0_sel:DWORD src1_sel:DWORD
	v_bitop3_b32 v123, v133, s20, v131 bitop3:0xc8
	v_mad_i64_i32 v[94:95], s[18:19], v160, s21, v[204:205]
	v_lshl_add_u64 v[94:95], v[94:95], 0, v[108:109]
	global_load_dwordx4 v[94:97], v[94:95], off
	s_waitcnt lgkmcnt(0)
	v_pk_mul_f32 v[126:127], v[86:87], v[92:93] op_sel_hi:[1,0]
	v_pk_mul_f32 v[86:87], v[64:65], v[100:101]
	v_pk_mul_f32 v[90:91], v[90:91], v[92:93] op_sel_hi:[1,0]
	v_pk_fma_f32 v[86:87], v[60:61], v[98:99], v[86:87]
	v_lshlrev_b32_e32 v98, 16, v104
	v_and_b32_e32 v99, 0xffff0000, v104
	v_pk_fma_f32 v[86:87], v[52:53], v[98:99], v[86:87]
	v_pk_mul_f32 v[88:89], v[88:89], v[92:93] op_sel_hi:[1,0]
	v_pk_add_f32 v[86:87], v[56:57], v[86:87]
	v_lshlrev_b32_e32 v100, 16, v105
	v_mul_f32_e32 v93, 0xbfb8aa3b, v86
	v_exp_f32_e32 v98, v93
	v_mul_f32_e32 v93, 0xbfb8aa3b, v87
	v_exp_f32_e32 v99, v93
	v_pk_mul_f32 v[92:93], v[84:85], v[92:93] op_sel_hi:[1,0]
	v_add_f32_e32 v84, 1.0, v98
	v_and_b32_e32 v101, 0xffff0000, v105
	v_add_f32_e32 v85, 1.0, v99
	v_pk_mul_f32 v[98:99], v[66:67], v[118:119]
	v_rcp_f32_e32 v84, v84
	v_pk_fma_f32 v[98:99], v[62:63], v[116:117], v[98:99]
	v_rcp_f32_e32 v85, v85
	v_pk_fma_f32 v[98:99], v[54:55], v[100:101], v[98:99]
	v_and_b32_dpp v117, v105, v164 row_ror:1 row_mask:0xf bank_mask:0xf bound_ctrl:1
	v_pk_add_f32 v[98:99], v[58:59], v[98:99]
	v_pk_mul_f32 v[84:85], v[86:87], v[84:85]
	v_mul_f32_e32 v100, 0xbfb8aa3b, v98
	v_mul_f32_e32 v101, 0xbfb8aa3b, v99
	v_exp_f32_e32 v100, v100
	v_exp_f32_e32 v101, v101
	v_pk_mul_f32 v[84:85], v[84:85], v[88:89]
	v_pk_mul_f32 v[88:89], v[48:49], v[102:103]
	v_add_f32_e32 v100, 1.0, v100
	v_add_f32_e32 v101, 1.0, v101
	v_rcp_f32_e32 v100, v100
	v_rcp_f32_e32 v101, v101
	v_pk_fma_f32 v[88:89], v[44:45], v[120:121], v[88:89]
	v_cvt_pk_bf16_f32 v84, v84, v85
	v_and_b32_dpp v105, v105, v161 row_ror:2 row_mask:0xf bank_mask:0xf bound_ctrl:1
	v_pk_mul_f32 v[86:87], v[98:99], v[100:101]
	v_lshlrev_b32_e32 v98, 16, v107
	v_pk_mul_f32 v[86:87], v[90:91], v[86:87]
	v_lshlrev_b32_e32 v90, 16, v106
	v_and_b32_e32 v91, 0xffff0000, v106
	v_pk_fma_f32 v[88:89], v[36:37], v[90:91], v[88:89]
	v_and_b32_e32 v99, 0xffff0000, v107
	v_pk_add_f32 v[88:89], v[40:41], v[88:89]
	v_and_b32_dpp v120, v106, v164 row_ror:1 row_mask:0xf bank_mask:0xf bound_ctrl:1
	v_mul_f32_e32 v85, 0xbfb8aa3b, v88
	v_exp_f32_e32 v90, v85
	v_mul_f32_e32 v85, 0xbfb8aa3b, v89
	v_exp_f32_e32 v91, v85
	v_cvt_pk_bf16_f32 v85, v86, v87
	v_add_f32_e32 v86, 1.0, v90
	v_rcp_f32_e32 v86, v86
	v_add_f32_e32 v87, 1.0, v91
	v_pk_mul_f32 v[90:91], v[50:51], v[124:125]
	v_rcp_f32_e32 v87, v87
	v_pk_fma_f32 v[90:91], v[46:47], v[122:123], v[90:91]
	v_and_b32_dpp v121, v106, v161 row_ror:2 row_mask:0xf bank_mask:0xf bound_ctrl:1
	v_pk_fma_f32 v[90:91], v[38:39], v[98:99], v[90:91]
	v_pk_mul_f32 v[86:87], v[88:89], v[86:87]
	v_pk_add_f32 v[90:91], v[42:43], v[90:91]
	v_pk_mul_f32 v[86:87], v[92:93], v[86:87]
	v_mul_f32_e32 v98, 0xbfb8aa3b, v90
	v_mul_f32_e32 v99, 0xbfb8aa3b, v91
	v_exp_f32_e32 v98, v98
	v_exp_f32_e32 v99, v99
	v_cvt_pk_bf16_f32 v86, v86, v87
	v_and_b32_dpp v93, v104, v161 row_ror:2 row_mask:0xf bank_mask:0xf bound_ctrl:1
	v_add_f32_e32 v98, 1.0, v98
	v_add_f32_e32 v99, 1.0, v99
	v_rcp_f32_e32 v98, v98
	v_rcp_f32_e32 v99, v99
	v_and_b32_dpp v124, v107, v164 row_ror:1 row_mask:0xf bank_mask:0xf bound_ctrl:1
	v_and_b32_dpp v107, v107, v161 row_ror:2 row_mask:0xf bank_mask:0xf bound_ctrl:1
	v_pk_mul_f32 v[88:89], v[90:91], v[98:99]
	s_nop 0
	v_pk_mul_f32 v[88:89], v[126:127], v[88:89]
	v_and_b32_dpp v99, v104, v164 row_ror:1 row_mask:0xf bank_mask:0xf bound_ctrl:1
	v_cvt_pk_bf16_f32 v87, v88, v89
	global_store_dwordx4 v[148:149], v[84:87], off offset:256
	v_mov_b32_e32 v88, v228
	s_nop 0
	v_mad_i64_i32 v[84:85], s[18:19], v152, s21, v[204:205]
	v_lshl_add_u64 v[84:85], v[84:85], 0, v[108:109]
	global_load_dwordx4 v[84:87], v[84:85], off
	s_waitcnt vmcnt(2)
	v_mov_b32_dpp v91, v94 row_shr:2 row_mask:0xf bank_mask:0xf bound_ctrl:1
	v_mov_b32_dpp v89, v94 row_shr:1 row_mask:0xf bank_mask:0xf bound_ctrl:1
	v_or_b32_sdwa v92, v93, v91 dst_sel:WORD_1 dst_unused:UNUSED_PAD src0_sel:DWORD src1_sel:DWORD
	v_mov_b32_dpp v103, v95 row_shr:1 row_mask:0xf bank_mask:0xf bound_ctrl:1
	v_mov_b32_dpp v101, v95 row_shr:2 row_mask:0xf bank_mask:0xf bound_ctrl:1
	v_mov_b32_dpp v118, v96 row_shr:1 row_mask:0xf bank_mask:0xf bound_ctrl:1
	v_mov_b32_dpp v119, v96 row_shr:2 row_mask:0xf bank_mask:0xf bound_ctrl:1
	v_bitop3_b32 v93, v93, s20, v91 bitop3:0xc8
	v_or_b32_sdwa v90, v99, v89 dst_sel:WORD_1 dst_unused:UNUSED_PAD src0_sel:DWORD src1_sel:DWORD
	v_or_b32_sdwa v98, v117, v103 dst_sel:WORD_1 dst_unused:UNUSED_PAD src0_sel:DWORD src1_sel:DWORD
	v_or_b32_sdwa v100, v105, v101 dst_sel:WORD_1 dst_unused:UNUSED_PAD src0_sel:DWORD src1_sel:DWORD
	v_or_b32_sdwa v102, v120, v118 dst_sel:WORD_1 dst_unused:UNUSED_PAD src0_sel:DWORD src1_sel:DWORD
	v_or_b32_sdwa v104, v121, v119 dst_sel:WORD_1 dst_unused:UNUSED_PAD src0_sel:DWORD src1_sel:DWORD
	v_bitop3_b32 v91, v99, s20, v89 bitop3:0xc8
	v_bitop3_b32 v101, v105, s20, v101 bitop3:0xc8
	v_bitop3_b32 v99, v117, s20, v103 bitop3:0xc8
	v_bitop3_b32 v105, v121, s20, v119 bitop3:0xc8
	v_bitop3_b32 v103, v120, s20, v118 bitop3:0xc8
	v_mov_b32_dpp v123, v97 row_shr:2 row_mask:0xf bank_mask:0xf bound_ctrl:1
	v_mov_b32_dpp v122, v97 row_shr:1 row_mask:0xf bank_mask:0xf bound_ctrl:1
	v_or_b32_sdwa v116, v107, v123 dst_sel:WORD_1 dst_unused:UNUSED_PAD src0_sel:DWORD src1_sel:DWORD
	v_bitop3_b32 v117, v107, s20, v123 bitop3:0xc8
	v_or_b32_sdwa v106, v124, v122 dst_sel:WORD_1 dst_unused:UNUSED_PAD src0_sel:DWORD src1_sel:DWORD
	v_bitop3_b32 v107, v124, s20, v122 bitop3:0xc8
	s_waitcnt lgkmcnt(0)
	v_pk_mul_f32 v[118:119], v[78:79], v[88:89] op_sel_hi:[1,0]
	v_pk_mul_f32 v[78:79], v[64:65], v[92:93]
	v_pk_mul_f32 v[82:83], v[82:83], v[88:89] op_sel_hi:[1,0]
	v_pk_fma_f32 v[78:79], v[60:61], v[90:91], v[78:79]
	v_lshlrev_b32_e32 v90, 16, v94
	v_and_b32_e32 v91, 0xffff0000, v94
	v_pk_fma_f32 v[78:79], v[52:53], v[90:91], v[78:79]
	v_pk_mul_f32 v[80:81], v[80:81], v[88:89] op_sel_hi:[1,0]
	v_pk_add_f32 v[78:79], v[56:57], v[78:79]
	v_lshlrev_b32_e32 v92, 16, v95
	v_mul_f32_e32 v89, 0xbfb8aa3b, v78
	v_exp_f32_e32 v90, v89
	v_mul_f32_e32 v89, 0xbfb8aa3b, v79
	v_exp_f32_e32 v91, v89
	v_pk_mul_f32 v[88:89], v[76:77], v[88:89] op_sel_hi:[1,0]
	v_add_f32_e32 v76, 1.0, v90
	v_and_b32_e32 v93, 0xffff0000, v95
	v_add_f32_e32 v77, 1.0, v91
	v_pk_mul_f32 v[90:91], v[66:67], v[100:101]
	v_rcp_f32_e32 v76, v76
	v_pk_fma_f32 v[90:91], v[62:63], v[98:99], v[90:91]
	v_rcp_f32_e32 v77, v77
	v_pk_fma_f32 v[90:91], v[54:55], v[92:93], v[90:91]
	s_waitcnt vmcnt(0)
	v_mov_b32_dpp v98, v86 row_shr:1 row_mask:0xf bank_mask:0xf bound_ctrl:1
	v_pk_add_f32 v[90:91], v[58:59], v[90:91]
	v_pk_mul_f32 v[76:77], v[78:79], v[76:77]
	v_mul_f32_e32 v92, 0xbfb8aa3b, v90
	v_mul_f32_e32 v93, 0xbfb8aa3b, v91
	v_exp_f32_e32 v92, v92
	v_exp_f32_e32 v93, v93
	v_pk_mul_f32 v[76:77], v[76:77], v[80:81]
	v_pk_mul_f32 v[80:81], v[48:49], v[104:105]
	v_add_f32_e32 v92, 1.0, v92
	v_add_f32_e32 v93, 1.0, v93
	v_rcp_f32_e32 v92, v92
	v_rcp_f32_e32 v93, v93
	v_pk_fma_f32 v[80:81], v[44:45], v[102:103], v[80:81]
	v_cvt_pk_bf16_f32 v76, v76, v77
	v_mov_b32_dpp v99, v86 row_shr:2 row_mask:0xf bank_mask:0xf bound_ctrl:1
	v_pk_mul_f32 v[78:79], v[90:91], v[92:93]
	v_lshlrev_b32_e32 v90, 16, v97
	v_pk_mul_f32 v[78:79], v[82:83], v[78:79]
	v_lshlrev_b32_e32 v82, 16, v96
	v_and_b32_e32 v83, 0xffff0000, v96
	v_pk_fma_f32 v[80:81], v[36:37], v[82:83], v[80:81]
	v_and_b32_e32 v91, 0xffff0000, v97
	v_pk_add_f32 v[80:81], v[40:41], v[80:81]
	v_mov_b32_dpp v92, v96 row_ror:2 row_mask:0xf bank_mask:0xf bound_ctrl:1
	v_mul_f32_e32 v77, 0xbfb8aa3b, v80
	v_exp_f32_e32 v82, v77
	v_mul_f32_e32 v77, 0xbfb8aa3b, v81
	v_exp_f32_e32 v83, v77
	v_cvt_pk_bf16_f32 v77, v78, v79
	v_add_f32_e32 v78, 1.0, v82
	v_rcp_f32_e32 v78, v78
	v_add_f32_e32 v79, 1.0, v83
	v_pk_mul_f32 v[82:83], v[50:51], v[116:117]
	v_rcp_f32_e32 v79, v79
	v_pk_fma_f32 v[82:83], v[46:47], v[106:107], v[82:83]
	v_cndmask_b32_e64 v101, 0, v92, s[38:39]
	v_pk_fma_f32 v[82:83], v[38:39], v[90:91], v[82:83]
	v_pk_mul_f32 v[78:79], v[80:81], v[78:79]
	v_pk_add_f32 v[82:83], v[42:43], v[82:83]
	v_pk_mul_f32 v[78:79], v[88:89], v[78:79]
	v_mul_f32_e32 v90, 0xbfb8aa3b, v82
	v_mul_f32_e32 v91, 0xbfb8aa3b, v83
	v_exp_f32_e32 v90, v90
	v_exp_f32_e32 v91, v91
	v_cvt_pk_bf16_f32 v78, v78, v79
	v_or_b32_sdwa v92, v101, v99 dst_sel:WORD_1 dst_unused:UNUSED_PAD src0_sel:DWORD src1_sel:DWORD
	v_add_f32_e32 v90, 1.0, v90
	v_add_f32_e32 v91, 1.0, v91
	v_rcp_f32_e32 v90, v90
	v_rcp_f32_e32 v91, v91
	v_mov_b32_dpp v88, v95 row_ror:2 row_mask:0xf bank_mask:0xf bound_ctrl:1
	v_mov_b32_dpp v89, v85 row_shr:2 row_mask:0xf bank_mask:0xf bound_ctrl:1
	v_mov_b32_dpp v103, v87 row_shr:2 row_mask:0xf bank_mask:0xf bound_ctrl:1
	v_pk_mul_f32 v[80:81], v[82:83], v[90:91]
	v_mov_b32_dpp v82, v95 row_ror:1 row_mask:0xf bank_mask:0xf bound_ctrl:1
	v_pk_mul_f32 v[80:81], v[118:119], v[80:81]
	v_mov_b32_dpp v90, v96 row_ror:1 row_mask:0xf bank_mask:0xf bound_ctrl:1
	v_cvt_pk_bf16_f32 v79, v80, v81
	global_store_dwordx4 v[142:143], v[76:79], off offset:256
	s_nop 1
	v_mov_b32_e32 v76, v229
	v_mov_b32_dpp v80, v94 row_ror:2 row_mask:0xf bank_mask:0xf bound_ctrl:1
	v_mov_b32_dpp v78, v94 row_ror:1 row_mask:0xf bank_mask:0xf bound_ctrl:1
	v_mov_b32_dpp v79, v84 row_shr:2 row_mask:0xf bank_mask:0xf bound_ctrl:1
	v_cndmask_b32_e64 v81, 0, v80, s[38:39]
	v_mov_b32_dpp v77, v84 row_shr:1 row_mask:0xf bank_mask:0xf bound_ctrl:1
	v_cndmask_b32_e64 v83, 0, v78, s[36:37]
	v_or_b32_sdwa v80, v81, v79 dst_sel:WORD_1 dst_unused:UNUSED_PAD src0_sel:DWORD src1_sel:DWORD
	v_mov_b32_dpp v91, v85 row_shr:1 row_mask:0xf bank_mask:0xf bound_ctrl:1
	v_cndmask_b32_e64 v93, 0, v82, s[36:37]
	v_cndmask_b32_e64 v100, 0, v90, s[36:37]
	v_bitop3_b32 v81, v81, s20, v79 bitop3:0xc8
	v_or_b32_sdwa v78, v83, v77 dst_sel:WORD_1 dst_unused:UNUSED_PAD src0_sel:DWORD src1_sel:DWORD
	v_or_b32_sdwa v82, v93, v91 dst_sel:WORD_1 dst_unused:UNUSED_PAD src0_sel:DWORD src1_sel:DWORD
	v_or_b32_sdwa v90, v100, v98 dst_sel:WORD_1 dst_unused:UNUSED_PAD src0_sel:DWORD src1_sel:DWORD
	v_bitop3_b32 v79, v83, s20, v77 bitop3:0xc8
	v_bitop3_b32 v83, v93, s20, v91 bitop3:0xc8
	v_bitop3_b32 v93, v101, s20, v99 bitop3:0xc8
	v_bitop3_b32 v91, v100, s20, v98 bitop3:0xc8
	v_cndmask_b32_e64 v95, 0, v88, s[38:39]
	v_or_b32_sdwa v88, v95, v89 dst_sel:WORD_1 dst_unused:UNUSED_PAD src0_sel:DWORD src1_sel:DWORD
	v_bitop3_b32 v89, v95, s20, v89 bitop3:0xc8
	v_mov_b32_dpp v96, v97 row_ror:2 row_mask:0xf bank_mask:0xf bound_ctrl:1
	v_mov_b32_dpp v94, v97 row_ror:1 row_mask:0xf bank_mask:0xf bound_ctrl:1
	v_cndmask_b32_e64 v97, 0, v96, s[38:39]
	v_mov_b32_dpp v102, v87 row_shr:1 row_mask:0xf bank_mask:0xf bound_ctrl:1
	v_cndmask_b32_e64 v104, 0, v94, s[36:37]
	v_or_b32_sdwa v96, v97, v103 dst_sel:WORD_1 dst_unused:UNUSED_PAD src0_sel:DWORD src1_sel:DWORD
	v_bitop3_b32 v97, v97, s20, v103 bitop3:0xc8
	v_or_b32_sdwa v94, v104, v102 dst_sel:WORD_1 dst_unused:UNUSED_PAD src0_sel:DWORD src1_sel:DWORD
	v_bitop3_b32 v95, v104, s20, v102 bitop3:0xc8
	s_waitcnt lgkmcnt(0)
	v_pk_mul_f32 v[98:99], v[70:71], v[76:77] op_sel_hi:[1,0]
	v_pk_mul_f32 v[70:71], v[64:65], v[80:81]
	v_pk_mul_f32 v[74:75], v[74:75], v[76:77] op_sel_hi:[1,0]
	v_pk_fma_f32 v[70:71], v[60:61], v[78:79], v[70:71]
	v_lshlrev_b32_e32 v78, 16, v84
	v_and_b32_e32 v79, 0xffff0000, v84
	v_pk_fma_f32 v[70:71], v[52:53], v[78:79], v[70:71]
	v_pk_mul_f32 v[72:73], v[72:73], v[76:77] op_sel_hi:[1,0]
	v_pk_add_f32 v[70:71], v[56:57], v[70:71]
	v_lshlrev_b32_e32 v80, 16, v85
	v_mul_f32_e32 v77, 0xbfb8aa3b, v70
	v_exp_f32_e32 v78, v77
	v_mul_f32_e32 v77, 0xbfb8aa3b, v71
	v_exp_f32_e32 v79, v77
	v_pk_mul_f32 v[76:77], v[68:69], v[76:77] op_sel_hi:[1,0]
	v_add_f32_e32 v68, 1.0, v78
	v_and_b32_e32 v81, 0xffff0000, v85
	v_add_f32_e32 v69, 1.0, v79
	v_pk_mul_f32 v[78:79], v[66:67], v[88:89]
	v_rcp_f32_e32 v68, v68
	v_pk_fma_f32 v[78:79], v[62:63], v[82:83], v[78:79]
	v_rcp_f32_e32 v69, v69
	v_pk_fma_f32 v[78:79], v[54:55], v[80:81], v[78:79]
	v_pk_mul_f32 v[68:69], v[70:71], v[68:69]
	v_pk_add_f32 v[78:79], v[58:59], v[78:79]
	v_pk_mul_f32 v[68:69], v[68:69], v[72:73]
	v_mul_f32_e32 v80, 0xbfb8aa3b, v78
	v_mul_f32_e32 v81, 0xbfb8aa3b, v79
	v_exp_f32_e32 v80, v80
	v_exp_f32_e32 v81, v81
	v_pk_mul_f32 v[72:73], v[48:49], v[92:93]
	v_cvt_pk_bf16_f32 v68, v68, v69
	v_add_f32_e32 v80, 1.0, v80
	v_add_f32_e32 v81, 1.0, v81
	v_rcp_f32_e32 v80, v80
	v_rcp_f32_e32 v81, v81
	v_pk_fma_f32 v[72:73], v[44:45], v[90:91], v[72:73]
	v_pk_mul_f32 v[70:71], v[78:79], v[80:81]
	s_nop 0
	v_pk_mul_f32 v[70:71], v[74:75], v[70:71]
	v_lshlrev_b32_e32 v74, 16, v86
	v_and_b32_e32 v75, 0xffff0000, v86
	v_pk_fma_f32 v[72:73], v[36:37], v[74:75], v[72:73]
	v_lshlrev_b32_e32 v78, 16, v87
	v_pk_add_f32 v[72:73], v[40:41], v[72:73]
	v_and_b32_e32 v79, 0xffff0000, v87
	v_mul_f32_e32 v69, 0xbfb8aa3b, v72
	v_exp_f32_e32 v74, v69
	v_mul_f32_e32 v69, 0xbfb8aa3b, v73
	v_exp_f32_e32 v75, v69
	v_cvt_pk_bf16_f32 v69, v70, v71
	v_add_f32_e32 v70, 1.0, v74
	v_rcp_f32_e32 v70, v70
	v_add_f32_e32 v71, 1.0, v75
	v_pk_mul_f32 v[74:75], v[50:51], v[96:97]
	v_rcp_f32_e32 v71, v71
	v_pk_fma_f32 v[74:75], v[46:47], v[94:95], v[74:75]
	v_pk_mul_f32 v[70:71], v[72:73], v[70:71]
	v_pk_fma_f32 v[74:75], v[38:39], v[78:79], v[74:75]
	v_pk_mul_f32 v[70:71], v[76:77], v[70:71]
	v_pk_add_f32 v[74:75], v[42:43], v[74:75]
	v_cvt_pk_bf16_f32 v70, v70, v71
	v_mul_f32_e32 v78, 0xbfb8aa3b, v74
	v_mul_f32_e32 v79, 0xbfb8aa3b, v75
	v_exp_f32_e32 v78, v78
	v_exp_f32_e32 v79, v79
	v_mad_i64_i32 v[76:77], s[18:19], v159, s21, v[204:205]
	v_add_f32_e32 v78, 1.0, v78
	v_add_f32_e32 v79, 1.0, v79
	v_rcp_f32_e32 v78, v78
	v_rcp_f32_e32 v79, v79
	v_lshl_add_u64 v[76:77], v[76:77], 0, v[108:109]
	v_pk_mul_f32 v[72:73], v[74:75], v[78:79]
	s_nop 0
	v_pk_mul_f32 v[72:73], v[98:99], v[72:73]
	s_nop 0
	v_cvt_pk_bf16_f32 v71, v72, v73
	v_mad_i64_i32 v[72:73], s[18:19], v165, s21, v[204:205]
	v_lshl_add_u64 v[72:73], v[72:73], 0, v[108:109]
	global_load_dwordx4 v[72:75], v[72:73], off
	s_nop 0
	global_store_dwordx4 v[136:137], v[68:71], off offset:256
	global_load_dwordx4 v[68:71], v[140:141], off offset:256
	s_nop 0
	global_load_dword v80, v[202:203], off offset:512
	global_load_dword v227, v[202:203], off offset:576
	global_load_dword v228, v[202:203], off offset:640
	global_load_dword v229, v[202:203], off offset:704
	s_waitcnt lgkmcnt(0)
	s_waitcnt vmcnt(6)
	v_mov_b32_dpp v83, v72 row_shr:2 row_mask:0xf bank_mask:0xf bound_ctrl:1
	v_mov_b32_dpp v81, v72 row_shr:1 row_mask:0xf bank_mask:0xf bound_ctrl:1
	s_waitcnt vmcnt(4)
	v_and_b32_dpp v87, v68, v157 row_ror:2 row_mask:0xf bank_mask:0xf bound_ctrl:1
	v_and_b32_dpp v85, v68, v158 row_ror:1 row_mask:0xf bank_mask:0xf bound_ctrl:1
	v_or_b32_sdwa v68, v87, v83 dst_sel:WORD_1 dst_unused:UNUSED_PAD src0_sel:DWORD src1_sel:DWORD
	v_mov_b32_dpp v89, v73 row_shr:1 row_mask:0xf bank_mask:0xf bound_ctrl:1
	v_mov_b32_dpp v91, v73 row_shr:2 row_mask:0xf bank_mask:0xf bound_ctrl:1
	v_and_b32_dpp v93, v69, v158 row_ror:1 row_mask:0xf bank_mask:0xf bound_ctrl:1
	v_and_b32_dpp v94, v69, v157 row_ror:2 row_mask:0xf bank_mask:0xf bound_ctrl:1
	v_mov_b32_dpp v95, v74 row_shr:1 row_mask:0xf bank_mask:0xf bound_ctrl:1
	v_and_b32_dpp v97, v70, v158 row_ror:1 row_mask:0xf bank_mask:0xf bound_ctrl:1
	v_bitop3_b32 v69, v87, s20, v83 bitop3:0xc8
	v_or_b32_sdwa v82, v85, v81 dst_sel:WORD_1 dst_unused:UNUSED_PAD src0_sel:DWORD src1_sel:DWORD
	v_or_b32_sdwa v84, v93, v89 dst_sel:WORD_1 dst_unused:UNUSED_PAD src0_sel:DWORD src1_sel:DWORD
	v_or_b32_sdwa v86, v94, v91 dst_sel:WORD_1 dst_unused:UNUSED_PAD src0_sel:DWORD src1_sel:DWORD
	v_or_b32_sdwa v88, v97, v95 dst_sel:WORD_1 dst_unused:UNUSED_PAD src0_sel:DWORD src1_sel:DWORD
	v_bitop3_b32 v83, v85, s20, v81 bitop3:0xc8
	v_bitop3_b32 v87, v94, s20, v91 bitop3:0xc8
	v_bitop3_b32 v85, v93, s20, v89 bitop3:0xc8
	v_bitop3_b32 v89, v97, s20, v95 bitop3:0xc8
	s_waitcnt vmcnt(3)
	v_pk_mul_f32 v[94:95], v[30:31], v[80:81] op_sel_hi:[1,0]
	v_pk_mul_f32 v[30:31], v[64:65], v[68:69]
	v_lshlrev_b32_e32 v68, 16, v72
	v_pk_fma_f32 v[30:31], v[60:61], v[82:83], v[30:31]
	v_and_b32_e32 v69, 0xffff0000, v72
	v_pk_fma_f32 v[30:31], v[52:53], v[68:69], v[30:31]
	v_pk_mul_f32 v[34:35], v[34:35], v[80:81] op_sel_hi:[1,0]
	v_pk_add_f32 v[30:31], v[56:57], v[30:31]
	v_pk_mul_f32 v[32:33], v[32:33], v[80:81] op_sel_hi:[1,0]
	v_mul_f32_e32 v68, 0xbfb8aa3b, v30
	v_exp_f32_e32 v81, v68
	v_mul_f32_e32 v68, 0xbfb8aa3b, v31
	v_exp_f32_e32 v82, v68
	v_and_b32_e32 v83, 0xffff0000, v73
	v_pk_mul_f32 v[68:69], v[28:29], v[80:81] op_sel_hi:[1,0]
	v_add_f32_e32 v28, 1.0, v81
	v_pk_mul_f32 v[80:81], v[66:67], v[86:87]
	v_add_f32_e32 v29, 1.0, v82
	v_pk_fma_f32 v[80:81], v[62:63], v[84:85], v[80:81]
	v_lshlrev_b32_e32 v82, 16, v73
	v_pk_fma_f32 v[80:81], v[54:55], v[82:83], v[80:81]
	v_rcp_f32_e32 v28, v28
	v_pk_add_f32 v[80:81], v[58:59], v[80:81]
	v_rcp_f32_e32 v29, v29
	v_mul_f32_e32 v82, 0xbfb8aa3b, v80
	v_mul_f32_e32 v83, 0xbfb8aa3b, v81
	v_exp_f32_e32 v82, v82
	v_exp_f32_e32 v83, v83
	v_mov_b32_dpp v96, v74 row_shr:2 row_mask:0xf bank_mask:0xf bound_ctrl:1
	v_and_b32_dpp v98, v70, v157 row_ror:2 row_mask:0xf bank_mask:0xf bound_ctrl:1
	v_add_f32_e32 v82, 1.0, v82
	v_add_f32_e32 v83, 1.0, v83
	v_rcp_f32_e32 v82, v82
	v_rcp_f32_e32 v83, v83
	v_or_b32_sdwa v70, v98, v96 dst_sel:WORD_1 dst_unused:UNUSED_PAD src0_sel:DWORD src1_sel:DWORD
	v_and_b32_dpp v101, v71, v158 row_ror:1 row_mask:0xf bank_mask:0xf bound_ctrl:1
	v_and_b32_dpp v102, v71, v157 row_ror:2 row_mask:0xf bank_mask:0xf bound_ctrl:1
	v_bitop3_b32 v71, v98, s20, v96 bitop3:0xc8
	v_pk_mul_f32 v[28:29], v[30:31], v[28:29]
	v_pk_mul_f32 v[30:31], v[80:81], v[82:83]
	v_pk_mul_f32 v[28:29], v[28:29], v[32:33]
	v_pk_mul_f32 v[32:33], v[48:49], v[70:71]
	v_pk_mul_f32 v[30:31], v[34:35], v[30:31]
	v_pk_fma_f32 v[32:33], v[44:45], v[88:89], v[32:33]
	v_lshlrev_b32_e32 v34, 16, v74
	v_and_b32_e32 v35, 0xffff0000, v74
	v_pk_fma_f32 v[32:33], v[36:37], v[34:35], v[32:33]
	v_cvt_pk_bf16_f32 v28, v28, v29
	v_pk_add_f32 v[32:33], v[40:41], v[32:33]
	v_mov_b32_dpp v100, v75 row_shr:2 row_mask:0xf bank_mask:0xf bound_ctrl:1
	v_mul_f32_e32 v29, 0xbfb8aa3b, v32
	v_exp_f32_e32 v34, v29
	v_mul_f32_e32 v29, 0xbfb8aa3b, v33
	v_exp_f32_e32 v35, v29
	v_mov_b32_dpp v99, v75 row_shr:1 row_mask:0xf bank_mask:0xf bound_ctrl:1
	v_or_b32_sdwa v92, v102, v100 dst_sel:WORD_1 dst_unused:UNUSED_PAD src0_sel:DWORD src1_sel:DWORD
	v_bitop3_b32 v93, v102, s20, v100 bitop3:0xc8
	v_or_b32_sdwa v90, v101, v99 dst_sel:WORD_1 dst_unused:UNUSED_PAD src0_sel:DWORD src1_sel:DWORD
	v_bitop3_b32 v91, v101, s20, v99 bitop3:0xc8
	v_cvt_pk_bf16_f32 v29, v30, v31
	v_add_f32_e32 v30, 1.0, v34
	v_add_f32_e32 v31, 1.0, v35
	v_pk_mul_f32 v[34:35], v[50:51], v[92:93]
	v_lshlrev_b32_e32 v70, 16, v75
	v_pk_fma_f32 v[34:35], v[46:47], v[90:91], v[34:35]
	v_and_b32_e32 v71, 0xffff0000, v75
	v_pk_fma_f32 v[34:35], v[38:39], v[70:71], v[34:35]
	v_rcp_f32_e32 v30, v30
	v_pk_add_f32 v[34:35], v[42:43], v[34:35]
	v_rcp_f32_e32 v31, v31
	v_mul_f32_e32 v70, 0xbfb8aa3b, v34
	v_mul_f32_e32 v71, 0xbfb8aa3b, v35
	v_exp_f32_e32 v70, v70
	v_exp_f32_e32 v71, v71
	v_pk_mul_f32 v[30:31], v[32:33], v[30:31]
	global_load_dwordx4 v[76:79], v[76:77], off
	v_add_f32_e32 v70, 1.0, v70
	v_add_f32_e32 v71, 1.0, v71
	v_rcp_f32_e32 v70, v70
	v_rcp_f32_e32 v71, v71
	v_pk_mul_f32 v[30:31], v[68:69], v[30:31]
	v_and_b32_dpp v69, v72, v154 row_ror:2 row_mask:0xf bank_mask:0xf bound_ctrl:1
	v_cvt_pk_bf16_f32 v30, v30, v31
	v_pk_mul_f32 v[32:33], v[34:35], v[70:71]
	v_and_b32_dpp v71, v72, v155 row_ror:1 row_mask:0xf bank_mask:0xf bound_ctrl:1
	v_pk_mul_f32 v[32:33], v[94:95], v[32:33]
	v_and_b32_dpp v85, v73, v155 row_ror:1 row_mask:0xf bank_mask:0xf bound_ctrl:1
	v_cvt_pk_bf16_f32 v31, v32, v33
	global_store_dwordx4 v[138:139], v[28:31], off offset:256
	s_waitcnt vmcnt(4)
	v_mov_b32_e32 v32, v227
	v_and_b32_dpp v88, v74, v155 row_ror:1 row_mask:0xf bank_mask:0xf bound_ctrl:1
	v_and_b32_dpp v89, v74, v154 row_ror:2 row_mask:0xf bank_mask:0xf bound_ctrl:1
	v_and_b32_dpp v92, v75, v155 row_ror:1 row_mask:0xf bank_mask:0xf bound_ctrl:1
	v_and_b32_dpp v93, v75, v154 row_ror:2 row_mask:0xf bank_mask:0xf bound_ctrl:1
	v_and_b32_dpp v73, v73, v154 row_ror:2 row_mask:0xf bank_mask:0xf bound_ctrl:1
	v_mad_i64_i32 v[28:29], s[18:19], v156, s21, v[204:205]
	v_lshl_add_u64 v[28:29], v[28:29], 0, v[108:109]
	global_load_dwordx4 v[28:31], v[28:29], off
	s_waitcnt lgkmcnt(0)
	s_waitcnt vmcnt(2)
	v_mov_b32_dpp v35, v76 row_shr:2 row_mask:0xf bank_mask:0xf bound_ctrl:1
	v_mov_b32_dpp v33, v76 row_shr:1 row_mask:0xf bank_mask:0xf bound_ctrl:1
	v_or_b32_sdwa v68, v69, v35 dst_sel:WORD_1 dst_unused:UNUSED_PAD src0_sel:DWORD src1_sel:DWORD
	v_mov_b32_dpp v81, v77 row_shr:1 row_mask:0xf bank_mask:0xf bound_ctrl:1
	v_mov_b32_dpp v86, v78 row_shr:1 row_mask:0xf bank_mask:0xf bound_ctrl:1
	v_mov_b32_dpp v87, v78 row_shr:2 row_mask:0xf bank_mask:0xf bound_ctrl:1
	v_bitop3_b32 v69, v69, s20, v35 bitop3:0xc8
	v_or_b32_sdwa v34, v71, v33 dst_sel:WORD_1 dst_unused:UNUSED_PAD src0_sel:DWORD src1_sel:DWORD
	v_or_b32_sdwa v70, v85, v81 dst_sel:WORD_1 dst_unused:UNUSED_PAD src0_sel:DWORD src1_sel:DWORD
	v_or_b32_sdwa v80, v88, v86 dst_sel:WORD_1 dst_unused:UNUSED_PAD src0_sel:DWORD src1_sel:DWORD
	v_or_b32_sdwa v74, v89, v87 dst_sel:WORD_1 dst_unused:UNUSED_PAD src0_sel:DWORD src1_sel:DWORD
	v_bitop3_b32 v35, v71, s20, v33 bitop3:0xc8
	v_bitop3_b32 v71, v85, s20, v81 bitop3:0xc8
	v_bitop3_b32 v75, v89, s20, v87 bitop3:0xc8
	v_bitop3_b32 v81, v88, s20, v86 bitop3:0xc8
	v_pk_mul_f32 v[86:87], v[22:23], v[32:33] op_sel_hi:[1,0]
	v_pk_mul_f32 v[22:23], v[64:65], v[68:69]
	v_pk_mul_f32 v[26:27], v[26:27], v[32:33] op_sel_hi:[1,0]
	v_pk_fma_f32 v[22:23], v[60:61], v[34:35], v[22:23]
	v_lshlrev_b32_e32 v34, 16, v76
	v_and_b32_e32 v35, 0xffff0000, v76
	v_pk_fma_f32 v[22:23], v[52:53], v[34:35], v[22:23]
	v_pk_mul_f32 v[24:25], v[24:25], v[32:33] op_sel_hi:[1,0]
	v_pk_add_f32 v[22:23], v[56:57], v[22:23]
	v_mov_b32_dpp v83, v77 row_shr:2 row_mask:0xf bank_mask:0xf bound_ctrl:1
	v_mul_f32_e32 v33, 0xbfb8aa3b, v22
	v_exp_f32_e32 v34, v33
	v_mul_f32_e32 v33, 0xbfb8aa3b, v23
	v_exp_f32_e32 v35, v33
	v_or_b32_sdwa v72, v73, v83 dst_sel:WORD_1 dst_unused:UNUSED_PAD src0_sel:DWORD src1_sel:DWORD
	v_bitop3_b32 v73, v73, s20, v83 bitop3:0xc8
	v_pk_mul_f32 v[32:33], v[20:21], v[32:33] op_sel_hi:[1,0]
	v_add_f32_e32 v20, 1.0, v34
	v_add_f32_e32 v21, 1.0, v35
	v_pk_mul_f32 v[34:35], v[66:67], v[72:73]
	v_lshlrev_b32_e32 v68, 16, v77
	v_pk_fma_f32 v[34:35], v[62:63], v[70:71], v[34:35]
	v_and_b32_e32 v69, 0xffff0000, v77
	v_pk_fma_f32 v[34:35], v[54:55], v[68:69], v[34:35]
	v_rcp_f32_e32 v20, v20
	v_pk_add_f32 v[34:35], v[58:59], v[34:35]
	v_rcp_f32_e32 v21, v21
	v_mul_f32_e32 v68, 0xbfb8aa3b, v34
	v_mul_f32_e32 v69, 0xbfb8aa3b, v35
	v_exp_f32_e32 v68, v68
	v_exp_f32_e32 v69, v69
	v_pk_mul_f32 v[20:21], v[22:23], v[20:21]
	v_mov_b32_dpp v91, v79 row_shr:2 row_mask:0xf bank_mask:0xf bound_ctrl:1
	v_add_f32_e32 v68, 1.0, v68
	v_add_f32_e32 v69, 1.0, v69
	v_rcp_f32_e32 v68, v68
	v_rcp_f32_e32 v69, v69
	v_pk_mul_f32 v[20:21], v[20:21], v[24:25]
	v_pk_mul_f32 v[24:25], v[48:49], v[74:75]
	v_cvt_pk_bf16_f32 v20, v20, v21
	v_pk_mul_f32 v[22:23], v[34:35], v[68:69]
	v_pk_fma_f32 v[24:25], v[44:45], v[80:81], v[24:25]
	v_pk_mul_f32 v[22:23], v[26:27], v[22:23]
	v_lshlrev_b32_e32 v26, 16, v78
	v_and_b32_e32 v27, 0xffff0000, v78
	v_pk_fma_f32 v[24:25], v[36:37], v[26:27], v[24:25]
	v_mov_b32_dpp v90, v79 row_shr:1 row_mask:0xf bank_mask:0xf bound_ctrl:1
	v_pk_add_f32 v[24:25], v[40:41], v[24:25]
	v_or_b32_sdwa v84, v93, v91 dst_sel:WORD_1 dst_unused:UNUSED_PAD src0_sel:DWORD src1_sel:DWORD
	v_mul_f32_e32 v21, 0xbfb8aa3b, v24
	v_exp_f32_e32 v26, v21
	v_mul_f32_e32 v21, 0xbfb8aa3b, v25
	v_exp_f32_e32 v27, v21
	v_bitop3_b32 v85, v93, s20, v91 bitop3:0xc8
	v_or_b32_sdwa v82, v92, v90 dst_sel:WORD_1 dst_unused:UNUSED_PAD src0_sel:DWORD src1_sel:DWORD
	v_bitop3_b32 v83, v92, s20, v90 bitop3:0xc8
	v_cvt_pk_bf16_f32 v21, v22, v23
	v_add_f32_e32 v22, 1.0, v26
	v_add_f32_e32 v23, 1.0, v27
	v_pk_mul_f32 v[26:27], v[50:51], v[84:85]
	v_lshlrev_b32_e32 v34, 16, v79
	v_pk_fma_f32 v[26:27], v[46:47], v[82:83], v[26:27]
	v_and_b32_e32 v35, 0xffff0000, v79
	v_pk_fma_f32 v[26:27], v[38:39], v[34:35], v[26:27]
	v_rcp_f32_e32 v22, v22
	v_pk_add_f32 v[26:27], v[42:43], v[26:27]
	v_rcp_f32_e32 v23, v23
	v_mul_f32_e32 v34, 0xbfb8aa3b, v26
	v_mul_f32_e32 v35, 0xbfb8aa3b, v27
	v_exp_f32_e32 v34, v34
	v_exp_f32_e32 v35, v35
	v_pk_mul_f32 v[22:23], v[24:25], v[22:23]
	v_and_b32_dpp v73, v77, v147 row_ror:1 row_mask:0xf bank_mask:0xf bound_ctrl:1
	v_add_f32_e32 v34, 1.0, v34
	v_add_f32_e32 v35, 1.0, v35
	v_rcp_f32_e32 v34, v34
	v_rcp_f32_e32 v35, v35
	v_pk_mul_f32 v[22:23], v[32:33], v[22:23]
	v_and_b32_dpp v33, v76, v146 row_ror:2 row_mask:0xf bank_mask:0xf bound_ctrl:1
	v_cvt_pk_bf16_f32 v22, v22, v23
	v_pk_mul_f32 v[24:25], v[26:27], v[34:35]
	v_and_b32_dpp v35, v76, v147 row_ror:1 row_mask:0xf bank_mask:0xf bound_ctrl:1
	v_pk_mul_f32 v[24:25], v[86:87], v[24:25]
	v_and_b32_dpp v75, v77, v146 row_ror:2 row_mask:0xf bank_mask:0xf bound_ctrl:1
	v_cvt_pk_bf16_f32 v23, v24, v25
	global_store_dwordx4 v[114:115], v[20:23], off offset:256
	v_mov_b32_e32 v24, v228
	v_and_b32_dpp v81, v78, v147 row_ror:1 row_mask:0xf bank_mask:0xf bound_ctrl:1
	v_mad_i64_i32 v[20:21], s[18:19], v153, s21, v[204:205]
	v_lshl_add_u64 v[20:21], v[20:21], 0, v[108:109]
	global_load_dwordx4 v[20:23], v[20:21], off
	s_waitcnt vmcnt(2)
	v_mov_b32_dpp v27, v28 row_shr:2 row_mask:0xf bank_mask:0xf bound_ctrl:1
	v_mov_b32_dpp v25, v28 row_shr:1 row_mask:0xf bank_mask:0xf bound_ctrl:1
	v_or_b32_sdwa v32, v33, v27 dst_sel:WORD_1 dst_unused:UNUSED_PAD src0_sel:DWORD src1_sel:DWORD
	v_mov_b32_dpp v71, v29 row_shr:1 row_mask:0xf bank_mask:0xf bound_ctrl:1
	v_mov_b32_dpp v77, v30 row_shr:1 row_mask:0xf bank_mask:0xf bound_ctrl:1
	v_mov_b32_dpp v80, v30 row_shr:2 row_mask:0xf bank_mask:0xf bound_ctrl:1
	v_and_b32_dpp v78, v78, v146 row_ror:2 row_mask:0xf bank_mask:0xf bound_ctrl:1
	v_mov_b32_dpp v83, v31 row_shr:2 row_mask:0xf bank_mask:0xf bound_ctrl:1
	v_and_b32_dpp v84, v79, v147 row_ror:1 row_mask:0xf bank_mask:0xf bound_ctrl:1
	v_and_b32_dpp v79, v79, v146 row_ror:2 row_mask:0xf bank_mask:0xf bound_ctrl:1
	v_bitop3_b32 v33, v33, s20, v27 bitop3:0xc8
	v_or_b32_sdwa v26, v35, v25 dst_sel:WORD_1 dst_unused:UNUSED_PAD src0_sel:DWORD src1_sel:DWORD
	v_or_b32_sdwa v34, v73, v71 dst_sel:WORD_1 dst_unused:UNUSED_PAD src0_sel:DWORD src1_sel:DWORD
	v_or_b32_sdwa v70, v81, v77 dst_sel:WORD_1 dst_unused:UNUSED_PAD src0_sel:DWORD src1_sel:DWORD
	v_or_b32_sdwa v72, v78, v80 dst_sel:WORD_1 dst_unused:UNUSED_PAD src0_sel:DWORD src1_sel:DWORD
	v_or_b32_sdwa v76, v79, v83 dst_sel:WORD_1 dst_unused:UNUSED_PAD src0_sel:DWORD src1_sel:DWORD
	v_bitop3_b32 v27, v35, s20, v25 bitop3:0xc8
	v_bitop3_b32 v35, v73, s20, v71 bitop3:0xc8
	v_bitop3_b32 v73, v78, s20, v80 bitop3:0xc8
	v_bitop3_b32 v71, v81, s20, v77 bitop3:0xc8
	v_bitop3_b32 v77, v79, s20, v83 bitop3:0xc8
	v_mov_b32_dpp v69, v29 row_shr:2 row_mask:0xf bank_mask:0xf bound_ctrl:1
	v_or_b32_sdwa v68, v75, v69 dst_sel:WORD_1 dst_unused:UNUSED_PAD src0_sel:DWORD src1_sel:DWORD
	v_bitop3_b32 v69, v75, s20, v69 bitop3:0xc8
	v_mov_b32_dpp v82, v31 row_shr:1 row_mask:0xf bank_mask:0xf bound_ctrl:1
	v_or_b32_sdwa v74, v84, v82 dst_sel:WORD_1 dst_unused:UNUSED_PAD src0_sel:DWORD src1_sel:DWORD
	v_bitop3_b32 v75, v84, s20, v82 bitop3:0xc8
	s_mov_b64 s[18:19], -1
	s_waitcnt lgkmcnt(0)
	v_pk_mul_f32 v[78:79], v[14:15], v[24:25] op_sel_hi:[1,0]
	v_pk_mul_f32 v[14:15], v[64:65], v[32:33]
	v_pk_mul_f32 v[18:19], v[18:19], v[24:25] op_sel_hi:[1,0]
	v_pk_fma_f32 v[14:15], v[60:61], v[26:27], v[14:15]
	v_lshlrev_b32_e32 v26, 16, v28
	v_and_b32_e32 v27, 0xffff0000, v28
	v_pk_fma_f32 v[14:15], v[52:53], v[26:27], v[14:15]
	v_pk_mul_f32 v[16:17], v[16:17], v[24:25] op_sel_hi:[1,0]
	v_pk_add_f32 v[14:15], v[56:57], v[14:15]
	v_lshlrev_b32_e32 v32, 16, v29
	v_mul_f32_e32 v25, 0xbfb8aa3b, v14
	v_exp_f32_e32 v26, v25
	v_mul_f32_e32 v25, 0xbfb8aa3b, v15
	v_exp_f32_e32 v27, v25
	v_pk_mul_f32 v[24:25], v[12:13], v[24:25] op_sel_hi:[1,0]
	v_add_f32_e32 v12, 1.0, v26
	v_and_b32_e32 v33, 0xffff0000, v29
	v_add_f32_e32 v13, 1.0, v27
	v_pk_mul_f32 v[26:27], v[66:67], v[68:69]
	v_rcp_f32_e32 v12, v12
	v_pk_fma_f32 v[26:27], v[62:63], v[34:35], v[26:27]
	v_rcp_f32_e32 v13, v13
	v_pk_fma_f32 v[26:27], v[54:55], v[32:33], v[26:27]
	s_waitcnt vmcnt(0)
	v_mov_b32_dpp v34, v22 row_shr:1 row_mask:0xf bank_mask:0xf bound_ctrl:1
	v_pk_add_f32 v[26:27], v[58:59], v[26:27]
	v_pk_mul_f32 v[12:13], v[14:15], v[12:13]
	v_mul_f32_e32 v32, 0xbfb8aa3b, v26
	v_mul_f32_e32 v33, 0xbfb8aa3b, v27
	v_exp_f32_e32 v32, v32
	v_exp_f32_e32 v33, v33
	v_pk_mul_f32 v[12:13], v[12:13], v[16:17]
	v_pk_mul_f32 v[16:17], v[48:49], v[72:73]
	v_add_f32_e32 v32, 1.0, v32
	v_add_f32_e32 v33, 1.0, v33
	v_rcp_f32_e32 v32, v32
	v_rcp_f32_e32 v33, v33
	v_pk_fma_f32 v[16:17], v[44:45], v[70:71], v[16:17]
	v_cvt_pk_bf16_f32 v12, v12, v13
	v_mov_b32_dpp v35, v22 row_shr:2 row_mask:0xf bank_mask:0xf bound_ctrl:1
	v_pk_mul_f32 v[14:15], v[26:27], v[32:33]
	v_lshlrev_b32_e32 v26, 16, v31
	v_pk_mul_f32 v[14:15], v[18:19], v[14:15]
	v_lshlrev_b32_e32 v18, 16, v30
	v_and_b32_e32 v19, 0xffff0000, v30
	v_pk_fma_f32 v[16:17], v[36:37], v[18:19], v[16:17]
	v_and_b32_e32 v27, 0xffff0000, v31
	v_pk_add_f32 v[16:17], v[40:41], v[16:17]
	v_mov_b32_dpp v71, v23 row_shr:2 row_mask:0xf bank_mask:0xf bound_ctrl:1
	v_mul_f32_e32 v13, 0xbfb8aa3b, v16
	v_exp_f32_e32 v18, v13
	v_mul_f32_e32 v13, 0xbfb8aa3b, v17
	v_exp_f32_e32 v19, v13
	v_cvt_pk_bf16_f32 v13, v14, v15
	v_add_f32_e32 v14, 1.0, v18
	v_rcp_f32_e32 v14, v14
	v_add_f32_e32 v15, 1.0, v19
	v_pk_mul_f32 v[18:19], v[50:51], v[76:77]
	v_rcp_f32_e32 v15, v15
	v_pk_fma_f32 v[18:19], v[46:47], v[74:75], v[18:19]
	v_mov_b32_dpp v70, v23 row_shr:1 row_mask:0xf bank_mask:0xf bound_ctrl:1
	v_pk_fma_f32 v[18:19], v[38:39], v[26:27], v[18:19]
	v_pk_mul_f32 v[14:15], v[16:17], v[14:15]
	v_pk_add_f32 v[18:19], v[42:43], v[18:19]
	v_pk_mul_f32 v[14:15], v[24:25], v[14:15]
	v_mul_f32_e32 v26, 0xbfb8aa3b, v18
	v_mul_f32_e32 v27, 0xbfb8aa3b, v19
	v_exp_f32_e32 v26, v26
	v_exp_f32_e32 v27, v27
	v_cvt_pk_bf16_f32 v14, v14, v15
	v_mov_b32_dpp v24, v29 row_ror:2 row_mask:0xf bank_mask:0xf bound_ctrl:1
	v_add_f32_e32 v26, 1.0, v26
	v_add_f32_e32 v27, 1.0, v27
	v_rcp_f32_e32 v26, v26
	v_rcp_f32_e32 v27, v27
	v_mov_b32_dpp v25, v21 row_shr:2 row_mask:0xf bank_mask:0xf bound_ctrl:1
	v_cndmask_b32_e64 v33, 0, v24, s[38:39]
	v_or_b32_sdwa v24, v33, v25 dst_sel:WORD_1 dst_unused:UNUSED_PAD src0_sel:DWORD src1_sel:DWORD
	v_pk_mul_f32 v[16:17], v[18:19], v[26:27]
	v_mov_b32_dpp v18, v29 row_ror:1 row_mask:0xf bank_mask:0xf bound_ctrl:1
	v_pk_mul_f32 v[16:17], v[78:79], v[16:17]
	v_mov_b32_dpp v26, v30 row_ror:1 row_mask:0xf bank_mask:0xf bound_ctrl:1
	v_cvt_pk_bf16_f32 v15, v16, v17
	global_store_dwordx4 v[112:113], v[12:15], off offset:256
	s_nop 1
	v_mov_b32_e32 v12, v229
	v_mov_b32_dpp v16, v28 row_ror:2 row_mask:0xf bank_mask:0xf bound_ctrl:1
	v_mov_b32_dpp v14, v28 row_ror:1 row_mask:0xf bank_mask:0xf bound_ctrl:1
	v_mov_b32_dpp v15, v20 row_shr:2 row_mask:0xf bank_mask:0xf bound_ctrl:1
	v_cndmask_b32_e64 v17, 0, v16, s[38:39]
	v_mov_b32_dpp v28, v30 row_ror:2 row_mask:0xf bank_mask:0xf bound_ctrl:1
	v_mov_b32_dpp v13, v20 row_shr:1 row_mask:0xf bank_mask:0xf bound_ctrl:1
	v_cndmask_b32_e64 v19, 0, v14, s[36:37]
	v_or_b32_sdwa v16, v17, v15 dst_sel:WORD_1 dst_unused:UNUSED_PAD src0_sel:DWORD src1_sel:DWORD
	v_mov_b32_dpp v27, v21 row_shr:1 row_mask:0xf bank_mask:0xf bound_ctrl:1
	v_cndmask_b32_e64 v29, 0, v18, s[36:37]
	v_cndmask_b32_e64 v68, 0, v26, s[36:37]
	v_cndmask_b32_e64 v69, 0, v28, s[38:39]
	v_bitop3_b32 v17, v17, s20, v15 bitop3:0xc8
	v_or_b32_sdwa v14, v19, v13 dst_sel:WORD_1 dst_unused:UNUSED_PAD src0_sel:DWORD src1_sel:DWORD
	v_or_b32_sdwa v18, v29, v27 dst_sel:WORD_1 dst_unused:UNUSED_PAD src0_sel:DWORD src1_sel:DWORD
	v_or_b32_sdwa v26, v68, v34 dst_sel:WORD_1 dst_unused:UNUSED_PAD src0_sel:DWORD src1_sel:DWORD
	v_or_b32_sdwa v28, v69, v35 dst_sel:WORD_1 dst_unused:UNUSED_PAD src0_sel:DWORD src1_sel:DWORD
	v_bitop3_b32 v15, v19, s20, v13 bitop3:0xc8
	v_bitop3_b32 v19, v29, s20, v27 bitop3:0xc8
	v_bitop3_b32 v29, v69, s20, v35 bitop3:0xc8
	v_bitop3_b32 v27, v68, s20, v34 bitop3:0xc8
	v_bitop3_b32 v25, v33, s20, v25 bitop3:0xc8
	v_mov_b32_dpp v30, v31 row_ror:1 row_mask:0xf bank_mask:0xf bound_ctrl:1
	v_mov_b32_dpp v31, v31 row_ror:2 row_mask:0xf bank_mask:0xf bound_ctrl:1
	v_cndmask_b32_e64 v31, 0, v31, s[38:39]
	v_cndmask_b32_e64 v72, 0, v30, s[36:37]
	v_or_b32_sdwa v32, v31, v71 dst_sel:WORD_1 dst_unused:UNUSED_PAD src0_sel:DWORD src1_sel:DWORD
	v_bitop3_b32 v33, v31, s20, v71 bitop3:0xc8
	v_or_b32_sdwa v30, v72, v70 dst_sel:WORD_1 dst_unused:UNUSED_PAD src0_sel:DWORD src1_sel:DWORD
	v_bitop3_b32 v31, v72, s20, v70 bitop3:0xc8
	s_waitcnt lgkmcnt(0)
	v_pk_mul_f32 v[34:35], v[6:7], v[12:13] op_sel_hi:[1,0]
	v_pk_mul_f32 v[6:7], v[64:65], v[16:17]
	v_pk_mul_f32 v[10:11], v[10:11], v[12:13] op_sel_hi:[1,0]
	v_pk_fma_f32 v[6:7], v[60:61], v[14:15], v[6:7]
	v_lshlrev_b32_e32 v14, 16, v20
	v_and_b32_e32 v15, 0xffff0000, v20
	v_pk_fma_f32 v[6:7], v[52:53], v[14:15], v[6:7]
	v_pk_mul_f32 v[8:9], v[8:9], v[12:13] op_sel_hi:[1,0]
	v_pk_add_f32 v[6:7], v[56:57], v[6:7]
	v_lshlrev_b32_e32 v16, 16, v21
	v_mul_f32_e32 v13, 0xbfb8aa3b, v6
	v_exp_f32_e32 v14, v13
	v_mul_f32_e32 v13, 0xbfb8aa3b, v7
	v_exp_f32_e32 v15, v13
	v_pk_mul_f32 v[12:13], v[4:5], v[12:13] op_sel_hi:[1,0]
	v_add_f32_e32 v4, 1.0, v14
	v_and_b32_e32 v17, 0xffff0000, v21
	v_add_f32_e32 v5, 1.0, v15
	v_pk_mul_f32 v[14:15], v[66:67], v[24:25]
	v_rcp_f32_e32 v4, v4
	v_pk_fma_f32 v[14:15], v[62:63], v[18:19], v[14:15]
	v_rcp_f32_e32 v5, v5
	v_pk_fma_f32 v[14:15], v[54:55], v[16:17], v[14:15]
	v_pk_mul_f32 v[4:5], v[6:7], v[4:5]
	v_pk_add_f32 v[14:15], v[58:59], v[14:15]
	v_pk_mul_f32 v[4:5], v[4:5], v[8:9]
	v_mul_f32_e32 v16, 0xbfb8aa3b, v14
	v_mul_f32_e32 v17, 0xbfb8aa3b, v15
	v_exp_f32_e32 v16, v16
	v_exp_f32_e32 v17, v17
	v_pk_mul_f32 v[8:9], v[48:49], v[28:29]
	v_cvt_pk_bf16_f32 v4, v4, v5
	v_add_f32_e32 v16, 1.0, v16
	v_add_f32_e32 v17, 1.0, v17
	v_rcp_f32_e32 v16, v16
	v_rcp_f32_e32 v17, v17
	v_pk_fma_f32 v[8:9], v[44:45], v[26:27], v[8:9]
	v_pk_mul_f32 v[6:7], v[14:15], v[16:17]
	s_nop 0
	v_pk_mul_f32 v[6:7], v[10:11], v[6:7]
	v_lshlrev_b32_e32 v10, 16, v22
	v_and_b32_e32 v11, 0xffff0000, v22
	v_pk_fma_f32 v[8:9], v[36:37], v[10:11], v[8:9]
	v_lshlrev_b32_e32 v14, 16, v23
	v_pk_add_f32 v[8:9], v[40:41], v[8:9]
	v_and_b32_e32 v15, 0xffff0000, v23
	v_mul_f32_e32 v5, 0xbfb8aa3b, v8
	v_exp_f32_e32 v10, v5
	v_mul_f32_e32 v5, 0xbfb8aa3b, v9
	v_exp_f32_e32 v11, v5
	v_cvt_pk_bf16_f32 v5, v6, v7
	v_add_f32_e32 v6, 1.0, v10
	v_rcp_f32_e32 v6, v6
	v_add_f32_e32 v7, 1.0, v11
	v_pk_mul_f32 v[10:11], v[50:51], v[32:33]
	v_rcp_f32_e32 v7, v7
	v_pk_fma_f32 v[10:11], v[46:47], v[30:31], v[10:11]
	v_pk_mul_f32 v[6:7], v[8:9], v[6:7]
	v_pk_fma_f32 v[10:11], v[38:39], v[14:15], v[10:11]
	v_pk_mul_f32 v[6:7], v[12:13], v[6:7]
	v_pk_add_f32 v[10:11], v[42:43], v[10:11]
	v_cvt_pk_bf16_f32 v6, v6, v7
	v_mul_f32_e32 v14, 0xbfb8aa3b, v10
	v_mul_f32_e32 v15, 0xbfb8aa3b, v11
	v_exp_f32_e32 v14, v14
	v_exp_f32_e32 v15, v15
	v_add_f32_e32 v14, 1.0, v14
	v_add_f32_e32 v15, 1.0, v15
	v_rcp_f32_e32 v14, v14
	v_rcp_f32_e32 v15, v15
	s_nop 0
	v_pk_mul_f32 v[8:9], v[10:11], v[14:15]
	s_nop 0
	v_pk_mul_f32 v[8:9], v[34:35], v[8:9]
	s_nop 0
	v_cvt_pk_bf16_f32 v7, v8, v9
	global_store_dwordx4 v[110:111], v[4:7], off offset:256
	s_cbranch_vccnz .LBB0_1916
	s_andn2_b64 vcc, exec, s[0:1]
	s_cbranch_vccnz .LBB0_1915
	s_barrier
	s_branch .LBB0_1915
.LBB0_1926:
	s_waitcnt vmcnt(0)
	s_movk_i32 s20, 0x110
	v_mov_b32_e32 v241, 0x358637bd
	v_mov_b32_e32 v227, 0x3b808081
	v_mov_b32_e32 v228, 1
	v_mov_b32_e32 v229, 0xff800000
	s_barrier
